# attention loop hosts the fp8 conversion of expert-weight items [0,6912) (quarter item per 3rd iteration, vmcnt-accounted), prologue no longer converts them
# speedup vs baseline: 1.0152x; 1.0006x over previous
; __device__ __forceinline__ void f8w_convert_all(Frame& F) {
;     const int gw = F.vcu * NWAVES + F.wave, NGW = F.G * NWAVES;
;     const int h0 = (F.G == 256) ? F8W_HOST0 : 4 * F8_NTILES, h1 = h0 + F8W_HOSTED * NGW + F8W_IDLE * 1024 + F8W_BARQ * F8W_BARW;
;     const int g0 = (F.G == 256) ? F8W_HOST0 - F8W_BARQ0 * F8W_BARW : 4 * F8_NTILES;
;     for (int q = gw; q < 4 * F8_NTILES; q += NGW) { if (q >= g0 && q < h1) continue; const F8WItem it = f8w_item(F, q); f32x4 v[16];
.LBB0_148:
	v_readlane_b32 s86, v254, 10
	s_cmp_gt_i32 s0, 0x107ff
	v_readlane_b32 s87, v254, 11
	s_barrier
	s_cbranch_scc1 .LBB0_157
	s_lshl_b32 s2, s33, 5
	s_cmpk_eq_i32 s33, 0x100
	s_mov_b32 s1, 0x8400
	s_cselect_b32 s3, s1, 0x10800
	s_movk_i32 s1, 0
	s_cselect_b32 s1, s1, 0x10800
	s_add_i32 s5, s2, s3
	s_addk_i32 s5, 0x6180
	s_bfe_u32 s8, s68, 0x20006
	v_lshlrev_b32_e32 v1, 2, v6
	s_add_u32 s9, s58, 0x41400000
	v_and_b32_e32 v1, 60, v1
	s_addc_u32 s10, s59, 0
	v_lshl_or_b32 v74, s8, 6, v1
	v_and_b32_e32 v75, 48, v6
	s_add_u32 s11, s58, 0x2b400000
	v_lshlrev_b32_e32 v76, 12, v75
	v_lshlrev_b32_e32 v77, 6, v74
	s_addc_u32 s12, s59, 0
	s_mov_b32 s3, 0
	s_add_i32 s13, 0, 0x200d8
	v_mov_b32_e32 v71, 0
	s_movk_i32 s14, 0xc8
	s_mov_b32 s15, 0xc3e00000
	v_mov_b32_e32 v78, 0x43e00000
	s_branch .LBB0_152

; #define GAS __attribute__((address_space(1)))
; #define REPS(j) for (int rep_ = 0; rep_ < ((((REPMASK) >> (j)) & 1) ? 2 : 1); (++rep_, __syncthreads()))
; __device__ __forceinline__ F8WItem f8w_item(Frame& F, int q) {
;     const int tile = q >> 2, quarter = q & 3, le = tile / 528; int r = tile % 528; const int which = r / 176; r %= 176;
;     const int n4 = F.lane & 15, kq = F.lane >> 4; F8WItem it;
;     if (which < 2) { const int kb = r & 15, nb = (r >> 4) * 4 + quarter, n = 64 * nb + 4 * n4, pn = n >> 7, row = (n & 127) + which * 128;
;         it.src = INP(F, which == 0 ? I_EG : I_EU) + (size_t)le * DM * FF + (size_t)(64 * kb + 16 * kq) * FF + n; it.ld = FF;
;         it.dst = (GAS unsigned char*)(F.ws + WS_WGU) + (size_t)le * 5632 * DM + (size_t)(((pn * 8 + (kb >> 1)) * 2 + (kb & 1)) * 16384 + row * 64 + 16 * kq); }
;     else { const int kb = r % 44, nb = (r / 44) * 4 + quarter, n = 64 * nb + 4 * n4, pn = n >> 8, row = n & 255;
;         it.src = INP(F, I_ED) + (size_t)le * FF * DM + (size_t)(64 * kb + 16 * kq) * DM + n; it.ld = DM;
;         it.dst = (GAS unsigned char*)(F.ws + WS_WD) + (size_t)le * DM * FF + (size_t)(((pn * 22 + (kb >> 1)) * 2 + (kb & 1)) * 16384 + row * 64 + 16 * kq); }
;     return it;
; __global__ void __launch_bounds__(NTHR, 2) fwd_kernel(Args args) {
;     ...
;             __syncthreads();
;             float gq_ = fabsf(INP(F, I_QNORM)[l * 64 + F.lane]), gk_ = fabsf(INP(F, I_KNORM)[l * 64 + F.lane]);
;             gq_ = fmaxf(gq_, dpp_f<DPP_X1>(gq_)); gq_ = fmaxf(gq_, dpp_f<DPP_X2>(gq_)); gq_ = fmaxf(gq_, dpp_f<DPP_HMIR>(gq_)); gq_ = fmaxf(gq_, dpp_f<DPP_MIR>(gq_)); gq_ = swap16_max(gq_); gq_ = swap32_max(gq_);
;             gk_ = fmaxf(gk_, dpp_f<DPP_X1>(gk_)); gk_ = fmaxf(gk_, dpp_f<DPP_X2>(gk_)); gk_ = fmaxf(gk_, dpp_f<DPP_HMIR>(gk_)); gk_ = fmaxf(gk_, dpp_f<DPP_MIR>(gk_)); gk_ = swap16_max(gk_); gk_ = swap32_max(gk_);
;             const float mfix = __uint_as_float(__builtin_amdgcn_readfirstlane(__float_as_uint(1.02f * ATT_C2 * 64.0f * gq_ * gk_)));
;             const bool nomax = mfix <= 60.0f;
;             REPS(13) for (int i = 0; ; ++i) { const int U = split ? F.vcu + F.G * i : 2 * F.vcu + i; if (U >= 512 || (!split && i >= 2)) break;
;                     const int grp = U >> 6, j = U & 63, b = grp >> 1, h = (grp & 1) * 4 + (j >> 4), qb = j & 15;
.LBB0_711:
	v_readlane_b32 s2, v254, 36
	s_barrier
	s_nop 0
	v_mov_b32_e32 v1, s2
	s_barrier
	ds_read_b128 v[2:5], v1
	v_readlane_b32 s4, v255, 5
	s_andn2_b64 vcc, exec, s[10:11]
	s_mov_b64 s[46:47], 0x20000
	v_lshl_or_b32 v182, s4, 6, v186
	s_waitcnt lgkmcnt(0)
	v_readfirstlane_b32 s2, v2
	v_readfirstlane_b32 s3, v3
	v_lshlrev_b64 v[2:3], 2, v[182:183]
	s_waitcnt vmcnt(0)
	v_lshl_add_u64 v[6:7], s[2:3], 0, v[2:3]
	v_readfirstlane_b32 s2, v4
	v_readfirstlane_b32 s3, v5
	global_load_dword v1, v[6:7], off
	s_nop 0
	v_lshl_add_u64 v[2:3], s[2:3], 0, v[2:3]
	global_load_dword v2, v[2:3], off
	s_waitcnt vmcnt(0)
	v_and_b32_e32 v3, 0x7fffffff, v1
	s_nop 1
	v_mov_b32_dpp v3, v3 quad_perm:[1,0,3,2] row_mask:0xf bank_mask:0xf bound_ctrl:1
	v_max_f32_e64 v1, |v1|, |v1|
	v_and_b32_e32 v4, 0x7fffffff, v2
	v_max_f32_e32 v3, v3, v3
	v_max_f32_e64 v2, |v2|, |v2|
	v_mov_b32_dpp v4, v4 quad_perm:[1,0,3,2] row_mask:0xf bank_mask:0xf bound_ctrl:1
	v_max_f32_e32 v4, v4, v4
	v_max_f32_e32 v1, v1, v3
	v_max_f32_e32 v2, v2, v4
	s_nop 0
	v_mov_b32_dpp v3, v1 quad_perm:[2,3,0,1] row_mask:0xf bank_mask:0xf bound_ctrl:1
	v_mov_b32_dpp v4, v2 quad_perm:[2,3,0,1] row_mask:0xf bank_mask:0xf bound_ctrl:1
	v_max_f32_e32 v3, v3, v3
	v_max_f32_e32 v4, v4, v4
	v_max_f32_e32 v1, v1, v3
	v_max_f32_e32 v2, v2, v4
	s_nop 0
	v_mov_b32_dpp v3, v1 row_half_mirror row_mask:0xf bank_mask:0xf bound_ctrl:1
	v_mov_b32_dpp v4, v2 row_half_mirror row_mask:0xf bank_mask:0xf bound_ctrl:1
	v_max_f32_e32 v3, v3, v3
	v_max_f32_e32 v4, v4, v4
	v_max_f32_e32 v1, v1, v3
	v_max_f32_e32 v2, v2, v4
	s_nop 0
	v_mov_b32_dpp v3, v1 row_mirror row_mask:0xf bank_mask:0xf bound_ctrl:1
	v_mov_b32_dpp v4, v2 row_mirror row_mask:0xf bank_mask:0xf bound_ctrl:1
	v_max_f32_e32 v3, v3, v3
	v_max_f32_e32 v4, v4, v4
	v_max_f32_e32 v1, v1, v3
	v_max_f32_e32 v2, v2, v4
	v_mov_b32_e32 v3, v1
	v_mov_b32_e32 v4, v2
	s_nop 0
	v_permlane16_swap_b32_e32 v1, v3
	v_permlane16_swap_b32_e32 v2, v4
	v_max_f32_e32 v3, v3, v3
	v_max_f32_e32 v1, v1, v1
	v_max_f32_e32 v4, v4, v4
	v_max_f32_e32 v2, v2, v2
	v_max_f32_e32 v1, v1, v3
	v_max_f32_e32 v2, v2, v4
	v_mov_b32_e32 v3, v1
	v_mov_b32_e32 v4, v2
	s_nop 0
	v_permlane32_swap_b32_e32 v1, v3
	v_permlane32_swap_b32_e32 v2, v4
	v_max_f32_e32 v3, v3, v3
	v_max_f32_e32 v1, v1, v1
	v_max_f32_e32 v4, v4, v4
	v_max_f32_e32 v2, v2, v2
	v_max_f32_e32 v1, v1, v3
	v_max_f32_e32 v2, v2, v4
	v_mul_f32_e32 v1, 0x413c5bb7, v1
	v_mul_f32_e32 v1, v1, v2
	s_nop 0
	v_readfirstlane_b32 s34, v1
	s_cbranch_vccnz .LBB0_773
	s_lshl_b32 s3, s22, 1
	s_ashr_i32 s2, s22, 6
	s_or_b32 s35, s3, 1
	s_and_b32 s36, s3, 14
	s_ashr_i32 s3, s2, 31
	s_lshl_b64 s[8:9], s[2:3], 12
	s_lshl_b64 s[2:3], s[2:3], 21
	s_add_u32 s6, s58, s2
	s_addc_u32 s7, s59, s3
	s_lshl_b32 s10, s22, 2
	s_and_b32 s14, s10, 0x80
	s_add_u32 s6, s6, s14
	s_addc_u32 s7, s7, 0
	s_add_u32 s10, s6, 0xa400000
	s_addc_u32 s11, s7, 0
	s_add_u32 s12, s6, 0xa400100
	s_addc_u32 s13, s7, 0
	s_lshl_b32 s6, s22, 4
	s_and_b32 s6, s6, 0x380
	s_add_u32 s6, s58, s6
	s_addc_u32 s7, s59, 0
	s_add_u32 s37, s6, 0x9400000
	s_addc_u32 s38, s7, 0
	s_add_u32 s39, s6, 0xac00200
	s_addc_u32 s40, s7, 0
	s_or_b32 s2, s2, s14
	s_add_u32 s2, s58, s2
	s_addc_u32 s3, s59, s3
	s_add_u32 s14, s2, 0xa408000
	s_addc_u32 s15, s3, 0
	s_add_u32 s16, s2, 0xa408100
	s_addc_u32 s17, s3, 0
	v_mov_b32_e32 v1, 0x42700000
	s_add_u32 s18, s2, 0xa5d8000
	v_cmp_le_f32_e64 s[4:5], s34, v1
	s_addc_u32 s19, s3, 0
	s_mov_b32 s41, 0
	s_mov_b64 s[20:21], -1
	s_mov_b32 s94, m0
	v_readfirstlane_b32 s22, v0
	v_readlane_b32 s23, v255, 5
	s_lshr_b32 s22, s22, 6
	s_lshl_b32 s24, s88, 3
	s_add_i32 s22, s22, s24
	v_and_b32_e32 v243, 15, v186
	v_lshrrev_b32_e32 v235, 4, v186
	v_lshlrev_b32_e32 v243, 8, v243
	v_lshl_add_u32 v243, v235, 4, v243
	v_mov_b32_e32 v244, 0
	s_mov_b32 s82, 0
	s_mov_b32 s83, 0
	s_mov_b32 s93, 0
	s_mov_b32 s32, 0
	v_mov_b32_e32 v1, 0x200c8
	ds_read_b64 v[34:35], v1
	ds_read_b64 v[36:37], v1 offset:8
	ds_read_b64 v[38:39], v1 offset:16
	s_waitcnt lgkmcnt(0)
	s_cmp_lg_u32 s23, 0
	s_cbranch_scc1 .Lah_dec_end
.Lah_dec:
	s_cmp_lt_u32 s22, 0x1b00
	s_cbranch_scc0 .Lah_dec_end
	s_mov_b32 s24, s22
	s_and_b32 s25, s24, 3
	s_lshr_b32 s24, s24, 2
	s_lshr_b32 s26, s24, 4
	s_mul_i32 s26, s26, 0x7c2
	s_lshr_b32 s26, s26, 16
	s_mul_i32 s27, s26, 0x210
	s_sub_i32 s24, s24, s27
	s_cmp_ge_u32 s24, 0x160
	s_cbranch_scc1 .Lah_dec_down
	s_cmp_ge_u32 s24, 0xb0
	s_cselect_b32 s27, 1, 0
	s_mul_i32 s28, s27, 0xb0
	s_sub_i32 s24, s24, s28
	s_and_b32 s28, s24, 15
	s_lshr_b32 s24, s24, 4
	s_lshl_b32 s24, s24, 2
	s_or_b32 s24, s24, s25
	v_readfirstlane_b32 s2, v34
	v_readfirstlane_b32 s3, v35
	v_readfirstlane_b32 s6, v36
	v_readfirstlane_b32 s7, v37
	s_cmp_eq_u32 s27, 0
	s_cselect_b32 s2, s2, s6
	s_cselect_b32 s3, s3, s7
	s_mul_i32 s6, s26, 0xb00000
	s_mul_i32 s7, s28, 0xb0000
	s_add_u32 s6, s6, s7
	s_lshl_b32 s7, s24, 8
	s_add_u32 s6, s6, s7
	s_add_u32 s2, s2, s6
	s_addc_u32 s3, s3, 0
	s_movk_i32 s29, 0x2c00
	s_mul_i32 s6, s26, 0x580000
	s_lshr_b32 s7, s24, 1
	s_lshl_b32 s7, s7, 4
	s_add_i32 s7, s7, s28
	s_lshl_b32 s7, s7, 14
	s_add_u32 s6, s6, s7
	s_and_b32 s7, s24, 1
	s_lshl_b32 s7, s7, 12
	s_add_u32 s6, s6, s7
	s_lshl_b32 s7, s27, 13
	s_add_u32 s6, s6, s7
	s_add_u32 s30, s58, 0x2b400000
	s_addc_u32 s31, s59, 0
	s_add_u32 s30, s30, s6
	s_addc_u32 s31, s31, 0
	s_branch .Lah_dec_put
.Lah_dec_down:
	s_sub_i32 s24, s24, 0x160
	s_cmp_ge_u32 s24, 44
	s_cselect_b32 s27, 1, 0
	s_cmp_ge_u32 s24, 0x58
	s_cselect_b32 s28, 1, 0
	s_add_i32 s27, s27, s28
	s_cmp_ge_u32 s24, 0x84
	s_cselect_b32 s28, 1, 0
	s_add_i32 s27, s27, s28
	s_mul_i32 s28, s27, 44
	s_sub_i32 s28, s24, s28
	s_lshl_b32 s24, s27, 2
	s_or_b32 s24, s24, s25
	v_readfirstlane_b32 s2, v38
	v_readfirstlane_b32 s3, v39
	s_mul_i32 s6, s26, 0xb00000
	s_lshl_b32 s7, s28, 18
	s_add_u32 s6, s6, s7
	s_lshl_b32 s7, s24, 8
	s_add_u32 s6, s6, s7
	s_add_u32 s2, s2, s6
	s_addc_u32 s3, s3, 0
	s_movk_i32 s29, 0x1000
	s_mul_i32 s6, s26, 0x2c0000
	s_lshr_b32 s7, s24, 2
	s_mul_i32 s7, s7, 44
	s_add_i32 s7, s7, s28
	s_lshl_b32 s7, s7, 14
	s_add_u32 s6, s6, s7
	s_and_b32 s7, s24, 3
	s_lshl_b32 s7, s7, 12
	s_add_u32 s6, s6, s7
	s_add_u32 s30, s58, 0x41400000
	s_addc_u32 s31, s59, 0
	s_add_u32 s30, s30, s6
	s_addc_u32 s31, s31, 0
.Lah_dec_put:
	s_mov_b32 m0, s93
	s_nop 0
	v_writelane_b32 v244, s2, m0
	s_add_i32 s93, s93, 1
	s_nop 0
	s_mov_b32 m0, s93
	s_nop 0
	v_writelane_b32 v244, s3, m0
	s_add_i32 s93, s93, 1
	s_nop 0
	s_mov_b32 m0, s93
	s_nop 0
	v_writelane_b32 v244, s30, m0
	s_add_i32 s93, s93, 1
	s_nop 0
	s_mov_b32 m0, s93
	s_nop 0
	v_writelane_b32 v244, s31, m0
	s_add_i32 s93, s93, 1
	s_nop 0
	s_mov_b32 m0, s93
	s_nop 0
	v_writelane_b32 v244, s29, m0
	s_add_i32 s93, s93, 1
	s_add_i32 s83, s83, 4
	s_add_i32 s22, s22, 0x800
	s_cmp_lt_u32 s83, 16
	s_cbranch_scc1 .Lah_dec
.Lah_dec_end:
	s_mov_b32 m0, s94
	s_nop 1
	s_branch .LBB0_715

; #define GAS __attribute__((address_space(1)))
; __device__ __forceinline__ void f8w_load(const F8WItem& it, f32x4 (&v)[16]) {
; #pragma unroll
;     for (int i = 0; i < 16; ++i) { const GAS float* a = it.src + (size_t)i * it.ld; asm volatile("global_load_dwordx4 %0, %1, off nt" : "=v"(v[i]) : "v"(a) : "memory"); }
; }
.LBB0_717:
	s_mov_b32 s101, 0
	s_cmp_lg_u32 s32, 0
	s_cbranch_scc1 .Lah_nold_a
	s_cmp_lt_u32 s82, s83
	s_cbranch_scc0 .Lah_nold_a
	s_mov_b32 s101, 1
	s_mov_b32 s93, s82
	s_lshr_b32 s98, s93, 2
	s_mul_i32 s98, s98, 5
	s_and_b32 s93, s93, 3
	s_add_i32 s99, s98, 1
	s_add_i32 s100, s98, 4
	v_readlane_b32 s84, v244, s98
	v_readlane_b32 s85, v244, s99
	v_readlane_b32 s99, v244, s100
	v_and_b32_e32 v246, 48, v243
	v_lshrrev_b32_e32 v209, 4, v243
	s_mul_i32 s100, s99, s93
	s_lshl_b32 s100, s100, 2
	s_add_u32 s84, s84, s100
	s_addc_u32 s85, s85, 0
	v_mul_u32_u24_e32 v246, s99, v246
	v_and_b32_e32 v209, 0xf0, v209
	v_add_u32_e32 v246, v246, v209
	s_nop 0
	global_load_dwordx4 v[210:213], v246, s[84:85] nt
	s_add_u32 s84, s84, s99
	s_addc_u32 s85, s85, 0
	global_load_dwordx4 v[214:217], v246, s[84:85] nt
	s_add_u32 s84, s84, s99
	s_addc_u32 s85, s85, 0
	global_load_dwordx4 v[218:221], v246, s[84:85] nt
	s_add_u32 s84, s84, s99
	s_addc_u32 s85, s85, 0
	global_load_dwordx2 v[222:223], v246, s[84:85] nt
	global_load_dwordx2 v[234:235], v246, s[84:85] offset:8 nt
.Lah_nold_a:
	v_add_u32_e32 v195, s43, v190
	ds_read_b64_tr_b16 v[196:197], v195 offset:24576
	ds_read_b64_tr_b16 v[198:199], v195 offset:25088
	v_add_f32_e32 v86, v66, v67
	v_add_f32_e32 v86, v68, v86
	v_add_f32_e32 v86, v69, v86
	v_add_f32_e32 v86, v70, v86
	v_add_f32_e32 v86, v71, v86
	v_cvt_pk_bf16_f32 v158, v66, v67
	v_cvt_pk_bf16_f32 v159, v68, v69
	s_waitcnt lgkmcnt(9)
	v_mfma_f32_32x32x16_bf16 v[98:113], v[82:85], v[154:157], v[34:49]
	ds_read_b64_tr_b16 v[66:67], v195 offset:28672
	ds_read_b64_tr_b16 v[68:69], v195 offset:29184
	v_add_f32_e32 v82, v72, v86
	v_add_f32_e32 v82, v73, v82
	v_add_f32_e32 v82, v74, v82
	v_add_f32_e32 v138, v75, v82
	s_waitcnt lgkmcnt(10)
	v_mfma_f32_32x32x16_bf16 v[82:97], v[166:169], v[154:157], v[34:49]
	v_cvt_pk_bf16_f32 v160, v70, v71
	v_cvt_pk_bf16_f32 v161, v72, v73
	ds_read_b64_tr_b16 v[70:71], v195 offset:25600
	ds_read_b64_tr_b16 v[72:73], v195 offset:26112
	v_add_f32_e32 v138, v76, v138
	v_add_f32_e32 v138, v77, v138
	v_add_f32_e32 v138, v78, v138
	v_add_f32_e32 v138, v79, v138
	v_cvt_pk_bf16_f32 v150, v74, v75
	v_cvt_pk_bf16_f32 v151, v76, v77
	s_waitcnt lgkmcnt(11)
	v_mfma_f32_32x32x16_bf16 v[98:113], v[170:173], v[146:149], v[98:113]
	ds_read_b64_tr_b16 v[74:75], v195 offset:29696
	ds_read_b64_tr_b16 v[76:77], v195 offset:30208
	s_waitcnt lgkmcnt(12)
	v_mfma_f32_32x32x16_bf16 v[82:97], v[162:165], v[146:149], v[82:97]
	v_add_f32_e32 v138, v80, v138
	v_add_f32_e32 v138, v81, v138
	v_add_f32_e32 v138, v50, v138
	v_add_f32_e32 v138, v51, v138
	v_cvt_pk_bf16_f32 v152, v78, v79
	v_cvt_pk_bf16_f32 v153, v80, v81
	ds_read_b64_tr_b16 v[78:79], v195 offset:26624
	ds_read_b64_tr_b16 v[80:81], v195 offset:27136
	s_waitcnt lgkmcnt(13)
	v_mfma_f32_32x32x16_bf16 v[98:113], v[126:129], v[134:137], v[98:113]
	v_add_f32_e32 v126, v52, v138
	v_add_f32_e32 v126, v53, v126
	v_add_f32_e32 v126, v54, v126
	v_add_f32_e32 v126, v55, v126
	v_cvt_pk_bf16_f32 v142, v50, v51
	v_cvt_pk_bf16_f32 v143, v52, v53
	ds_read_b64_tr_b16 v[50:51], v195 offset:30720
	ds_read_b64_tr_b16 v[52:53], v195 offset:31232
	s_waitcnt lgkmcnt(14)
	v_mfma_f32_32x32x16_bf16 v[82:97], v[122:125], v[134:137], v[82:97]
	v_add_f32_e32 v122, v56, v126
	v_add_f32_e32 v122, v57, v122
	v_add_f32_e32 v122, v58, v122
	v_add_f32_e32 v122, v59, v122
	v_cvt_pk_bf16_f32 v144, v54, v55
	v_cvt_pk_bf16_f32 v145, v56, v57
	ds_read_b64_tr_b16 v[54:55], v195 offset:27648
	ds_read_b64_tr_b16 v[56:57], v195 offset:28160
	s_waitcnt lgkmcnt(14)
	v_mfma_f32_32x32x16_bf16 v[98:113], v[118:121], v[130:133], v[98:113]
	v_add_f32_e32 v118, v60, v122
	v_add_f32_e32 v118, v61, v118
	v_add_f32_e32 v118, v62, v118
	v_add_f32_e32 v118, v63, v118
	v_cvt_pk_bf16_f32 v138, v58, v59
	v_cvt_pk_bf16_f32 v139, v60, v61
	ds_read_b64_tr_b16 v[58:59], v195 offset:31744
	ds_read_b64_tr_b16 v[60:61], v195 offset:32256
	v_mfma_f32_32x32x16_bf16 v[82:97], v[114:117], v[130:133], v[82:97]
	v_add_f32_e32 v114, v64, v118
	v_add_f32_e32 v114, v65, v114
	v_add_f32_e32 v195, 0, v114
	v_cvt_pk_bf16_f32 v140, v62, v63
	v_cvt_pk_bf16_f32 v141, v64, v65
	v_lshl_add_u64 v[62:63], v[178:179], 0, s[60:61]
	s_add_i32 s2, s42, s27
	s_mov_b32 s3, m0
	s_mov_b32 m0, s2
	s_nop 0
	global_load_lds_dwordx4 v[62:63], off
	s_mov_b32 m0, s3
	v_lshl_add_u64 v[62:63], v[180:181], 0, s[52:53]
	s_add_i32 s2, s31, s26
	s_mov_b32 s3, m0
	s_mov_b32 m0, s2
	s_nop 0
	global_load_lds_dwordx4 v[62:63], off
	s_mov_b32 m0, s3
	s_waitcnt lgkmcnt(14)
	v_mfma_f32_32x32x16_bf16 v[2:17], v[158:161], v[196:199], v[2:17]
	v_exp_f32_e32 v98, v98
	v_exp_f32_e32 v99, v99
	v_exp_f32_e32 v100, v100
	v_exp_f32_e32 v101, v101
	s_waitcnt lgkmcnt(12)
	v_mfma_f32_32x32x16_bf16 v[18:33], v[158:161], v[66:69], v[18:33]
	v_exp_f32_e32 v102, v102
	v_exp_f32_e32 v103, v103
	v_exp_f32_e32 v104, v104
	v_exp_f32_e32 v105, v105
	v_add_u32_e32 v66, s31, v191
	ds_read_b128 v[62:65], v66
	ds_read_b128 v[118:121], v66 offset:512
	s_waitcnt lgkmcnt(12)
	v_mfma_f32_32x32x16_bf16 v[2:17], v[150:153], v[70:73], v[2:17]
	v_exp_f32_e32 v106, v106
	v_exp_f32_e32 v107, v107
	v_exp_f32_e32 v108, v108
	v_exp_f32_e32 v109, v109
	ds_read_b128 v[122:125], v66 offset:2048
	ds_read_b128 v[126:129], v66 offset:2560
	s_waitcnt lgkmcnt(12)
	v_mfma_f32_32x32x16_bf16 v[18:33], v[150:153], v[74:77], v[18:33]
	v_exp_f32_e32 v110, v110
	v_exp_f32_e32 v111, v111
	v_exp_f32_e32 v112, v112
	v_exp_f32_e32 v113, v113
	ds_read_b128 v[162:165], v66 offset:4096
	ds_read_b128 v[166:169], v66 offset:4608
	s_waitcnt lgkmcnt(12)
	v_mfma_f32_32x32x16_bf16 v[2:17], v[142:145], v[78:81], v[2:17]
	v_exp_f32_e32 v82, v82
	v_exp_f32_e32 v83, v83
	v_exp_f32_e32 v84, v84
	v_exp_f32_e32 v85, v85
	ds_read_b128 v[170:173], v66 offset:6144
	ds_read_b128 v[114:117], v66 offset:6656
	s_waitcnt lgkmcnt(12)
	v_mfma_f32_32x32x16_bf16 v[18:33], v[142:145], v[50:53], v[18:33]
	v_exp_f32_e32 v86, v86
	v_exp_f32_e32 v87, v87
	v_exp_f32_e32 v88, v88
	v_exp_f32_e32 v89, v89
	s_waitcnt lgkmcnt(10)
	v_mfma_f32_32x32x16_bf16 v[2:17], v[138:141], v[54:57], v[2:17]
	v_exp_f32_e32 v90, v90
	v_exp_f32_e32 v91, v91
	v_exp_f32_e32 v92, v92
	v_exp_f32_e32 v93, v93
	s_waitcnt lgkmcnt(8)
	v_mfma_f32_32x32x16_bf16 v[18:33], v[138:141], v[58:61], v[18:33]
	v_exp_f32_e32 v94, v94
	v_exp_f32_e32 v95, v95
	v_exp_f32_e32 v96, v96
	v_exp_f32_e32 v97, v97
	s_cmp_lg_u32 s101, 0
	s_cbranch_scc1 .Lah_w7_a
	s_waitcnt vmcnt(2) lgkmcnt(0)
	s_branch .Lah_wd_a
; #define WAIT_BAR(N) asm volatile("s_waitcnt vmcnt(" #N ") lgkmcnt(0)\n\ts_barrier":::"memory")
;   #define RESC() do{ if(resc){ asm volatile("s_waitcnt lgkmcnt(0)":::"memory"); \
;       _Pragma("unroll") for(int d_=0;d_<2;++d_) _Pragma("unroll") for(int r=0;r<16;++r)o[d_][r]*=wsf[crow(r,hi)]; } }while(0)
;   #define ROT() do{sl_prev=sl_cur;sl_cur=sl_next;sl_next=(sl_next==(NSLOT-1)*SLOTB)?0:sl_next+SLOTB;}while(0)
;     ...
;   int t=1;
;     ...
;   for(;t+5<NT;t+=2){
;     STEP(pB0,pB1,pA0,pA1,t,true,true,true);     WAIT_BAR(2); RESC(); ROT();
.Lah_w7_a:
	s_waitcnt vmcnt(7) lgkmcnt(0)
.Lah_wd_a:
	s_barrier
	s_add_i32 s2, s31, 0x2000
	s_cmpk_lg_i32 s31, 0x4000
	s_cselect_b32 s2, s2, 0
	v_add_u32_e32 v204, s42, v190
	ds_read_b64_tr_b16 v[196:197], v204 offset:24576
	ds_read_b64_tr_b16 v[198:199], v204 offset:25088
	s_waitcnt lgkmcnt(9)
	v_mfma_f32_32x32x16_bf16 v[66:81], v[62:65], v[154:157], v[34:49]
	v_add_f32_e32 v50, v98, v99
	v_add_f32_e32 v50, v100, v50
	v_add_f32_e32 v50, v101, v50
	v_add_f32_e32 v50, v102, v50
	v_add_f32_e32 v50, v103, v50
	v_cvt_pk_bf16_f32 v158, v98, v99
	v_cvt_pk_bf16_f32 v159, v100, v101
	ds_read_b64_tr_b16 v[98:99], v204 offset:28672
	ds_read_b64_tr_b16 v[100:101], v204 offset:29184
	v_add_f32_e32 v50, v104, v50
	v_add_f32_e32 v50, v105, v50
	v_add_f32_e32 v50, v106, v50
	v_add_f32_e32 v138, v107, v50
	s_waitcnt lgkmcnt(10)
	v_mfma_f32_32x32x16_bf16 v[50:65], v[118:121], v[154:157], v[34:49]
	v_cvt_pk_bf16_f32 v160, v102, v103
	v_cvt_pk_bf16_f32 v161, v104, v105
	ds_read_b64_tr_b16 v[102:103], v204 offset:25600
	ds_read_b64_tr_b16 v[104:105], v204 offset:26112
	s_waitcnt lgkmcnt(11)
	v_mfma_f32_32x32x16_bf16 v[66:81], v[122:125], v[146:149], v[66:81]
	v_add_f32_e32 v118, v108, v138
	v_add_f32_e32 v118, v109, v118
	v_add_f32_e32 v118, v110, v118
	v_add_f32_e32 v118, v111, v118
	v_cvt_pk_bf16_f32 v150, v106, v107
	v_cvt_pk_bf16_f32 v151, v108, v109
	ds_read_b64_tr_b16 v[106:107], v204 offset:29696
	ds_read_b64_tr_b16 v[108:109], v204 offset:30208
	s_waitcnt lgkmcnt(12)
	v_mfma_f32_32x32x16_bf16 v[50:65], v[126:129], v[146:149], v[50:65]
	v_add_f32_e32 v118, v112, v118
	v_add_f32_e32 v118, v113, v118
	v_add_f32_e32 v118, v82, v118
	v_add_f32_e32 v118, v83, v118
	v_cvt_pk_bf16_f32 v152, v110, v111
	v_cvt_pk_bf16_f32 v153, v112, v113
	ds_read_b64_tr_b16 v[110:111], v204 offset:26624
	ds_read_b64_tr_b16 v[112:113], v204 offset:27136
	s_waitcnt lgkmcnt(13)
	v_mfma_f32_32x32x16_bf16 v[66:81], v[162:165], v[134:137], v[66:81]
	v_add_f32_e32 v118, v84, v118
	v_add_f32_e32 v118, v85, v118
	v_add_f32_e32 v118, v86, v118
	v_add_f32_e32 v118, v87, v118
	v_cvt_pk_bf16_f32 v142, v82, v83
	v_cvt_pk_bf16_f32 v143, v84, v85
	ds_read_b64_tr_b16 v[200:201], v204 offset:30720
	ds_read_b64_tr_b16 v[202:203], v204 offset:31232
	s_waitcnt lgkmcnt(14)
	v_mfma_f32_32x32x16_bf16 v[50:65], v[166:169], v[134:137], v[50:65]
	v_add_f32_e32 v82, v88, v118
	v_add_f32_e32 v82, v89, v82
	v_add_f32_e32 v82, v90, v82
	v_add_f32_e32 v82, v91, v82
	v_cvt_pk_bf16_f32 v144, v86, v87
	v_cvt_pk_bf16_f32 v145, v88, v89
	ds_read_b64_tr_b16 v[86:87], v204 offset:27648
	ds_read_b64_tr_b16 v[88:89], v204 offset:28160
	s_waitcnt lgkmcnt(14)
	v_mfma_f32_32x32x16_bf16 v[66:81], v[170:173], v[130:133], v[66:81]
	v_add_f32_e32 v82, v92, v82
	v_add_f32_e32 v82, v93, v82
	v_add_f32_e32 v82, v94, v82
	v_add_f32_e32 v82, v95, v82
	v_cvt_pk_bf16_f32 v138, v90, v91
	v_cvt_pk_bf16_f32 v139, v92, v93
	ds_read_b64_tr_b16 v[90:91], v204 offset:31744
	ds_read_b64_tr_b16 v[92:93], v204 offset:32256
	v_mfma_f32_32x32x16_bf16 v[50:65], v[114:117], v[130:133], v[50:65]
	v_add_f32_e32 v82, v96, v82
	v_add_f32_e32 v82, v97, v82
	v_add_f32_e32 v204, 0, v82
	v_cvt_pk_bf16_f32 v140, v94, v95
	v_cvt_pk_bf16_f32 v141, v96, v97
	v_lshl_add_u64 v[82:83], v[178:179], 0, s[46:47]
	s_add_i32 s3, s31, s27
	s_mov_b32 s22, m0
	s_mov_b32 m0, s3
	s_nop 0
	global_load_lds_dwordx4 v[82:83], off
	s_mov_b32 m0, s22
	v_lshl_add_u64 v[180:181], v[180:181], 0, s[54:55]
	s_add_i32 s3, s2, s26
	s_mov_b32 s22, m0
	s_mov_b32 m0, s3
	s_nop 0
	global_load_lds_dwordx4 v[180:181], off
	s_mov_b32 m0, s22
	s_waitcnt lgkmcnt(14)
	v_mfma_f32_32x32x16_bf16 v[2:17], v[158:161], v[196:199], v[2:17]
	v_exp_f32_e32 v66, v66
	v_exp_f32_e32 v67, v67
	v_exp_f32_e32 v68, v68
	v_exp_f32_e32 v69, v69
	s_waitcnt lgkmcnt(12)
	v_mfma_f32_32x32x16_bf16 v[18:33], v[158:161], v[98:101], v[18:33]
	v_exp_f32_e32 v70, v70
	v_exp_f32_e32 v71, v71
	v_exp_f32_e32 v72, v72
	v_exp_f32_e32 v73, v73
	v_add_u32_e32 v94, s2, v191
	ds_read_b128 v[82:85], v94
	ds_read_b128 v[166:169], v94 offset:512
	s_waitcnt lgkmcnt(12)
	v_mfma_f32_32x32x16_bf16 v[2:17], v[150:153], v[102:105], v[2:17]
	v_exp_f32_e32 v74, v74
	v_exp_f32_e32 v75, v75
	v_exp_f32_e32 v76, v76
	v_exp_f32_e32 v77, v77
	ds_read_b128 v[170:173], v94 offset:2048
	ds_read_b128 v[162:165], v94 offset:2560
	s_waitcnt lgkmcnt(12)
	v_mfma_f32_32x32x16_bf16 v[18:33], v[150:153], v[106:109], v[18:33]
	v_exp_f32_e32 v78, v78
	v_exp_f32_e32 v79, v79
	v_exp_f32_e32 v80, v80
	v_exp_f32_e32 v81, v81
	ds_read_b128 v[126:129], v94 offset:4096
	ds_read_b128 v[122:125], v94 offset:4608
	s_waitcnt lgkmcnt(12)
	v_mfma_f32_32x32x16_bf16 v[2:17], v[142:145], v[110:113], v[2:17]
	v_exp_f32_e32 v50, v50
	v_exp_f32_e32 v51, v51
	v_exp_f32_e32 v52, v52
	v_exp_f32_e32 v53, v53
	ds_read_b128 v[118:121], v94 offset:6144
	ds_read_b128 v[114:117], v94 offset:6656
	s_waitcnt lgkmcnt(12)
	v_mfma_f32_32x32x16_bf16 v[18:33], v[142:145], v[200:203], v[18:33]
	v_exp_f32_e32 v54, v54
	v_exp_f32_e32 v55, v55
	v_exp_f32_e32 v56, v56
	v_exp_f32_e32 v57, v57
	s_waitcnt lgkmcnt(10)
	v_mfma_f32_32x32x16_bf16 v[2:17], v[138:141], v[86:89], v[2:17]
	v_exp_f32_e32 v58, v58
	v_exp_f32_e32 v59, v59
	v_exp_f32_e32 v60, v60
	v_exp_f32_e32 v61, v61
	s_waitcnt lgkmcnt(8)
	v_mfma_f32_32x32x16_bf16 v[18:33], v[138:141], v[90:93], v[18:33]
	v_exp_f32_e32 v62, v62
	v_exp_f32_e32 v63, v63
	v_exp_f32_e32 v64, v64
	v_exp_f32_e32 v65, v65
	s_add_i32 s3, s2, 0x2000
	s_waitcnt vmcnt(2) lgkmcnt(0)
	s_barrier
	s_cmp_lg_u32 s101, 0
	s_cbranch_scc0 .Lah_skip_a
; #define WAIT_BAR(N) asm volatile("s_waitcnt vmcnt(" #N ") lgkmcnt(0)\n\ts_barrier":::"memory")
;   #define RESC() do{ if(resc){ asm volatile("s_waitcnt lgkmcnt(0)":::"memory"); \
;       _Pragma("unroll") for(int d_=0;d_<2;++d_) _Pragma("unroll") for(int r=0;r<16;++r)o[d_][r]*=wsf[crow(r,hi)]; } }while(0)
;   #define ROT() do{sl_prev=sl_cur;sl_cur=sl_next;sl_next=(sl_next==(NSLOT-1)*SLOTB)?0:sl_next+SLOTB;}while(0)
;   #define ENDW(tt) do{ if((tt)+3<NT){WAIT_BAR(2);} else if((tt)+2<NT){WAIT_BAR(1);} else {WAIT_BAR(0);} }while(0)
; #define GAS __attribute__((address_space(1)))
;     ...
;   for(;t+5<NT;t+=2){
;     STEP(pB0,pB1,pA0,pA1,t,true,true,true);     WAIT_BAR(2); RESC(); ROT();
;     STEP(pA0,pA1,pB0,pB1,t+1,true,true,true);   WAIT_BAR(2); RESC(); ROT();
;   }
;     ...
;   for(;t+1<NT;t+=2){
;     STEP(pB0,pB1,pA0,pA1,t,(t+3<NT),(t+1<NT),(t+1<NT));       ENDW(t);   RESC(); ROT();
;     STEP(pA0,pA1,pB0,pB1,t+1,(t+4<NT),(t+2<NT),(t+2<NT));     ENDW(t+1); RESC(); ROT();
; __device__ __forceinline__ void f8w_finish(const F8WItem& it, f32x4 (&v)[16]) {
;     asm volatile("s_waitcnt vmcnt(0)" : "+v"(v[0]), "+v"(v[1]), "+v"(v[2]), "+v"(v[3]), "+v"(v[4]), "+v"(v[5]), "+v"(v[6]), "+v"(v[7]),
;                  "+v"(v[8]), "+v"(v[9]), "+v"(v[10]), "+v"(v[11]), "+v"(v[12]), "+v"(v[13]), "+v"(v[14]), "+v"(v[15]) :: "memory");
; #pragma unroll
;     for (int j = 0; j < 4; ++j) { v4u o;
;         o.x = pk4_f8(v[0][j] * W8_SCALE, v[1][j] * W8_SCALE, v[2][j] * W8_SCALE, v[3][j] * W8_SCALE); o.y = pk4_f8(v[4][j] * W8_SCALE, v[5][j] * W8_SCALE, v[6][j] * W8_SCALE, v[7][j] * W8_SCALE);
;         o.z = pk4_f8(v[8][j] * W8_SCALE, v[9][j] * W8_SCALE, v[10][j] * W8_SCALE, v[11][j] * W8_SCALE); o.w = pk4_f8(v[12][j] * W8_SCALE, v[13][j] * W8_SCALE, v[14][j] * W8_SCALE, v[15][j] * W8_SCALE);
;         *(GAS v4u*)(it.dst + j * 64) = o; }
; }
	s_lshr_b32 s98, s82, 2
	s_mul_i32 s98, s98, 5
	s_add_i32 s99, s98, 2
	s_add_i32 s100, s98, 3
	s_and_b32 s93, s82, 3
	v_readlane_b32 s84, v244, s99
	v_readlane_b32 s85, v244, s100
	s_lshl_b32 s93, s93, 2
	v_mul_f32_e32 v210, 0x42800000, v210
	v_mul_f32_e32 v211, 0x42800000, v211
	v_mul_f32_e32 v212, 0x42800000, v212
	v_mul_f32_e32 v213, 0x42800000, v213
	v_mul_f32_e32 v214, 0x42800000, v214
	v_mul_f32_e32 v215, 0x42800000, v215
	v_mul_f32_e32 v216, 0x42800000, v216
	v_mul_f32_e32 v217, 0x42800000, v217
	v_mul_f32_e32 v218, 0x42800000, v218
	v_mul_f32_e32 v219, 0x42800000, v219
	v_mul_f32_e32 v220, 0x42800000, v220
	v_mul_f32_e32 v221, 0x42800000, v221
	v_mul_f32_e32 v222, 0x42800000, v222
	v_mul_f32_e32 v223, 0x42800000, v223
	v_mul_f32_e32 v234, 0x42800000, v234
	v_mul_f32_e32 v235, 0x42800000, v235
	s_add_u32 s84, s84, s93
	s_addc_u32 s85, s85, 0
	v_med3_f32 v210, v210, s33, v226
	v_med3_f32 v211, v211, s33, v226
	v_med3_f32 v212, v212, s33, v226
	v_med3_f32 v213, v213, s33, v226
	v_med3_f32 v214, v214, s33, v226
	v_med3_f32 v215, v215, s33, v226
	v_med3_f32 v216, v216, s33, v226
	v_med3_f32 v217, v217, s33, v226
	v_med3_f32 v218, v218, s33, v226
	v_med3_f32 v219, v219, s33, v226
	v_med3_f32 v220, v220, s33, v226
	v_med3_f32 v221, v221, s33, v226
	v_med3_f32 v222, v222, s33, v226
	v_med3_f32 v223, v223, s33, v226
	v_med3_f32 v234, v234, s33, v226
	v_med3_f32 v235, v235, s33, v226
	v_cvt_pk_fp8_f32 v210, v210, v214
	v_cvt_pk_fp8_f32 v211, v211, v215
	v_cvt_pk_fp8_f32 v212, v212, v216
	v_cvt_pk_fp8_f32 v213, v213, v217
	v_cvt_pk_fp8_f32 v210, v218, v222 op_sel:[0,0,1]
	v_cvt_pk_fp8_f32 v211, v219, v223 op_sel:[0,0,1]
	v_cvt_pk_fp8_f32 v212, v220, v234 op_sel:[0,0,1]
	v_cvt_pk_fp8_f32 v213, v221, v235 op_sel:[0,0,1]
	global_store_dword v243, v210, s[84:85]
	global_store_dword v243, v211, s[84:85] offset:64
	global_store_dword v243, v212, s[84:85] offset:128
	global_store_dword v243, v213, s[84:85] offset:192
	s_add_i32 s82, s82, 1
.Lah_skip_a:
	s_add_i32 s32, s32, -1
	s_cmp_lt_i32 s32, 0
	s_cselect_b32 s32, 2, s32
	s_cmpk_lg_i32 s2, 0x4000
	v_add_f32_e32 v86, v182, v195
	s_mov_b32 s43, s31
	s_cselect_b32 s31, s3, 0
	s_add_i32 s30, s30, 2
	v_lshl_add_u64 v[178:179], v[178:179], 0, s[54:55]
	s_mov_b32 s42, s2
	v_add_f32_e32 v182, v86, v204
	s_cmp_gt_u32 s30, 56
	s_cbranch_scc0 .LBB0_717
	s_and_b32 s3, s29, 0x3fffffc0
	s_cmp_lg_u32 0, -1
	s_cselect_b32 s2, 0, 0
	s_add_i32 s22, s2, 0x6000
	s_lshl_b32 s3, s3, 2
	v_add_u32_e32 v86, s22, v193
	s_add_i32 s22, s3, 0
	v_add3_u32 v178, v86, v192, v194
	ds_read_b64_tr_b16 v[192:193], v190 offset:32768
	ds_read_b64_tr_b16 v[194:195], v190 offset:33280
	v_add_f32_e32 v86, v66, v67
	v_add_f32_e32 v86, v68, v86
	v_add_f32_e32 v86, v69, v86
	v_add_f32_e32 v86, v70, v86
	v_add_f32_e32 v86, v71, v86
	v_cvt_pk_bf16_f32 v158, v66, v67
	v_cvt_pk_bf16_f32 v159, v68, v69
	s_waitcnt lgkmcnt(9)
	v_mfma_f32_32x32x16_bf16 v[98:113], v[82:85], v[154:157], v[34:49]
	ds_read_b64_tr_b16 v[66:67], v190 offset:36864
	ds_read_b64_tr_b16 v[68:69], v190 offset:37376
	v_add_f32_e32 v82, v72, v86
	v_add_f32_e32 v82, v73, v82
	v_add_f32_e32 v82, v74, v82
	v_add_f32_e32 v138, v75, v82
	v_cvt_pk_bf16_f32 v160, v70, v71
	v_cvt_pk_bf16_f32 v161, v72, v73
	s_waitcnt lgkmcnt(10)
	v_mfma_f32_32x32x16_bf16 v[82:97], v[166:169], v[154:157], v[34:49]
	ds_read_b64_tr_b16 v[70:71], v190 offset:33792
	ds_read_b64_tr_b16 v[72:73], v190 offset:34304
	v_add_f32_e32 v138, v76, v138
	v_add_f32_e32 v138, v77, v138
	v_add_f32_e32 v138, v78, v138
	v_add_f32_e32 v138, v79, v138
	v_cvt_pk_bf16_f32 v150, v74, v75
	v_cvt_pk_bf16_f32 v151, v76, v77
	s_waitcnt lgkmcnt(11)
	v_mfma_f32_32x32x16_bf16 v[98:113], v[170:173], v[146:149], v[98:113]
	ds_read_b64_tr_b16 v[74:75], v190 offset:37888
	ds_read_b64_tr_b16 v[76:77], v190 offset:38400
	v_add_f32_e32 v138, v80, v138
	v_add_f32_e32 v138, v81, v138
	v_add_f32_e32 v138, v50, v138
	v_add_f32_e32 v138, v51, v138
	v_cvt_pk_bf16_f32 v152, v78, v79
	v_cvt_pk_bf16_f32 v153, v80, v81
	s_waitcnt lgkmcnt(12)
	v_mfma_f32_32x32x16_bf16 v[82:97], v[162:165], v[146:149], v[82:97]
	ds_read_b64_tr_b16 v[78:79], v190 offset:34816
	ds_read_b64_tr_b16 v[80:81], v190 offset:35328
	s_waitcnt lgkmcnt(13)
	v_mfma_f32_32x32x16_bf16 v[98:113], v[126:129], v[134:137], v[98:113]
	v_add_f32_e32 v126, v52, v138
	v_add_f32_e32 v126, v53, v126
	v_add_f32_e32 v126, v54, v126
	v_add_f32_e32 v126, v55, v126
	v_cvt_pk_bf16_f32 v142, v50, v51
	v_cvt_pk_bf16_f32 v143, v52, v53
	ds_read_b64_tr_b16 v[50:51], v190 offset:38912
	ds_read_b64_tr_b16 v[52:53], v190 offset:39424
	s_waitcnt lgkmcnt(14)
	v_mfma_f32_32x32x16_bf16 v[82:97], v[122:125], v[134:137], v[82:97]
	v_add_f32_e32 v122, v56, v126
	v_add_f32_e32 v122, v57, v122
	v_add_f32_e32 v122, v58, v122
	v_add_f32_e32 v122, v59, v122
	v_cvt_pk_bf16_f32 v144, v54, v55
	v_cvt_pk_bf16_f32 v145, v56, v57
	ds_read_b64_tr_b16 v[54:55], v190 offset:35840
	ds_read_b64_tr_b16 v[56:57], v190 offset:36352
	s_waitcnt lgkmcnt(14)
	v_mfma_f32_32x32x16_bf16 v[98:113], v[118:121], v[130:133], v[98:113]
	v_add_f32_e32 v118, v60, v122
	v_add_f32_e32 v118, v61, v118
	v_add_f32_e32 v118, v62, v118
	v_add_f32_e32 v118, v63, v118
	v_cvt_pk_bf16_f32 v138, v58, v59
	v_cvt_pk_bf16_f32 v139, v60, v61
	ds_read_b64_tr_b16 v[58:59], v190 offset:39936
	ds_read_b64_tr_b16 v[60:61], v190 offset:40448
	v_mfma_f32_32x32x16_bf16 v[82:97], v[114:117], v[130:133], v[82:97]
	v_add_f32_e32 v114, v64, v118
	v_add_f32_e32 v114, v65, v114
	v_add_f32_e32 v114, 0, v114
	v_cvt_pk_bf16_f32 v140, v62, v63
	v_cvt_pk_bf16_f32 v141, v64, v65
	s_mov_b64 s[30:31], 0x1f0000
	s_add_i32 s2, s2, s28
	v_lshl_add_u64 v[62:63], v[176:177], 0, s[30:31]
	s_add_i32 s3, s2, 0x4000
	s_mov_b32 s23, m0
	s_mov_b32 m0, s3
	s_nop 0
	global_load_lds_dwordx4 v[62:63], off
	s_mov_b32 m0, s23
	s_mov_b64 s[28:29], 0x1e0000
	v_lshl_add_u64 v[62:63], v[174:175], 0, s[28:29]
	s_mov_b32 s3, m0
	s_mov_b32 m0, s26
	s_nop 0
	global_load_lds_dwordx4 v[62:63], off
	s_mov_b32 m0, s3
	v_add_f32_e32 v179, v182, v114
	s_waitcnt lgkmcnt(14)
; #define WAIT_BAR(N) asm volatile("s_waitcnt vmcnt(" #N ") lgkmcnt(0)\n\ts_barrier":::"memory")
;   #define RESC() do{ if(resc){ asm volatile("s_waitcnt lgkmcnt(0)":::"memory"); \
;       _Pragma("unroll") for(int d_=0;d_<2;++d_) _Pragma("unroll") for(int r=0;r<16;++r)o[d_][r]*=wsf[crow(r,hi)]; } }while(0)
;   #define ROT() do{sl_prev=sl_cur;sl_cur=sl_next;sl_next=(sl_next==(NSLOT-1)*SLOTB)?0:sl_next+SLOTB;}while(0)
;   #define ENDW(tt) do{ if((tt)+3<NT){WAIT_BAR(2);} else if((tt)+2<NT){WAIT_BAR(1);} else {WAIT_BAR(0);} }while(0)
;     ...
;   int t=1;
;     ...
;   for(;t+5<NT;t+=2){
;     STEP(pB0,pB1,pA0,pA1,t,true,true,true);     WAIT_BAR(2); RESC(); ROT();
;     STEP(pA0,pA1,pB0,pB1,t+1,true,true,true);   WAIT_BAR(2); RESC(); ROT();
;   }
;     ...
;   for(;t+1<NT;t+=2){
;     STEP(pB0,pB1,pA0,pA1,t,(t+3<NT),(t+1<NT),(t+1<NT));       ENDW(t);   RESC(); ROT();
;     STEP(pA0,pA1,pB0,pB1,t+1,(t+4<NT),(t+2<NT),(t+2<NT));     ENDW(t+1); RESC(); ROT();
	v_mfma_f32_32x32x16_bf16 v[2:17], v[158:161], v[192:195], v[2:17]
	v_exp_f32_e32 v98, v98
	v_exp_f32_e32 v99, v99
	v_exp_f32_e32 v100, v100
	v_exp_f32_e32 v101, v101
	s_waitcnt lgkmcnt(12)
	v_mfma_f32_32x32x16_bf16 v[18:33], v[158:161], v[66:69], v[18:33]
	v_exp_f32_e32 v102, v102
	v_exp_f32_e32 v103, v103
	v_exp_f32_e32 v104, v104
	v_exp_f32_e32 v105, v105
	ds_read_b128 v[62:65], v191
	ds_read_b128 v[162:165], v191 offset:512
	s_waitcnt lgkmcnt(12)
	v_mfma_f32_32x32x16_bf16 v[2:17], v[150:153], v[70:73], v[2:17]
	v_exp_f32_e32 v106, v106
	v_exp_f32_e32 v107, v107
	v_exp_f32_e32 v108, v108
	v_exp_f32_e32 v109, v109
	ds_read_b128 v[70:73], v191 offset:2048
	ds_read_b128 v[166:169], v191 offset:2560
	s_waitcnt lgkmcnt(12)
	v_mfma_f32_32x32x16_bf16 v[18:33], v[150:153], v[74:77], v[18:33]
	v_exp_f32_e32 v110, v110
	v_exp_f32_e32 v111, v111
	v_exp_f32_e32 v112, v112
	v_exp_f32_e32 v113, v113
	ds_read_b128 v[74:77], v191 offset:4096
	ds_read_b128 v[170:173], v191 offset:4608
	s_waitcnt lgkmcnt(12)
	v_mfma_f32_32x32x16_bf16 v[2:17], v[142:145], v[78:81], v[2:17]
	v_exp_f32_e32 v82, v82
	v_exp_f32_e32 v83, v83
	v_exp_f32_e32 v84, v84
	v_exp_f32_e32 v85, v85
	ds_read_b128 v[78:81], v191 offset:6144
	ds_read_b128 v[66:69], v191 offset:6656
	s_waitcnt lgkmcnt(12)
	v_mfma_f32_32x32x16_bf16 v[18:33], v[142:145], v[50:53], v[18:33]
	v_exp_f32_e32 v86, v86
	v_exp_f32_e32 v87, v87
	v_exp_f32_e32 v88, v88
	v_exp_f32_e32 v89, v89
	s_waitcnt lgkmcnt(10)
	v_mfma_f32_32x32x16_bf16 v[2:17], v[138:141], v[54:57], v[2:17]
	v_exp_f32_e32 v90, v90
	v_exp_f32_e32 v91, v91
	v_exp_f32_e32 v92, v92
	v_exp_f32_e32 v93, v93
	s_waitcnt lgkmcnt(8)
	v_mfma_f32_32x32x16_bf16 v[18:33], v[138:141], v[58:61], v[18:33]
	v_exp_f32_e32 v94, v94
	v_exp_f32_e32 v95, v95
	v_exp_f32_e32 v96, v96
	v_exp_f32_e32 v97, v97
	s_waitcnt vmcnt(2) lgkmcnt(0)
	s_barrier
	ds_read_b64_tr_b16 v[192:193], v190 offset:40960
	ds_read_b64_tr_b16 v[194:195], v190 offset:41472
	v_add_f32_e32 v50, v98, v99
	v_add_f32_e32 v50, v100, v50
	v_add_f32_e32 v50, v101, v50
	v_add_f32_e32 v50, v102, v50
	v_add_f32_e32 v50, v103, v50
	v_cvt_pk_bf16_f32 v158, v98, v99
	v_cvt_pk_bf16_f32 v159, v100, v101
	s_waitcnt lgkmcnt(9)
	v_mfma_f32_32x32x16_bf16 v[114:129], v[62:65], v[154:157], v[34:49]
	ds_read_b64_tr_b16 v[98:99], v190 offset:45056
	ds_read_b64_tr_b16 v[100:101], v190 offset:45568
	v_add_f32_e32 v50, v104, v50
	v_add_f32_e32 v50, v105, v50
	v_add_f32_e32 v50, v106, v50
	v_add_f32_e32 v138, v107, v50
	s_waitcnt lgkmcnt(10)
	v_mfma_f32_32x32x16_bf16 v[50:65], v[162:165], v[154:157], v[34:49]
	v_cvt_pk_bf16_f32 v160, v102, v103
	v_cvt_pk_bf16_f32 v161, v104, v105
	ds_read_b64_tr_b16 v[102:103], v190 offset:41984
	ds_read_b64_tr_b16 v[104:105], v190 offset:42496
	s_waitcnt lgkmcnt(11)
	v_mfma_f32_32x32x16_bf16 v[114:129], v[70:73], v[146:149], v[114:129]
	v_add_f32_e32 v70, v108, v138
	v_add_f32_e32 v70, v109, v70
	v_add_f32_e32 v70, v110, v70
	v_add_f32_e32 v138, v111, v70
	v_cvt_pk_bf16_f32 v150, v106, v107
	v_cvt_pk_bf16_f32 v151, v108, v109
	ds_read_b64_tr_b16 v[70:71], v190 offset:46080
	ds_read_b64_tr_b16 v[72:73], v190 offset:46592
	s_waitcnt lgkmcnt(12)
	v_mfma_f32_32x32x16_bf16 v[50:65], v[166:169], v[146:149], v[50:65]
	v_add_f32_e32 v106, v112, v138
	v_add_f32_e32 v106, v113, v106
	v_add_f32_e32 v106, v82, v106
	v_add_f32_e32 v138, v83, v106
	v_cvt_pk_bf16_f32 v152, v110, v111
	v_cvt_pk_bf16_f32 v153, v112, v113
	ds_read_b64_tr_b16 v[106:107], v190 offset:43008
	ds_read_b64_tr_b16 v[108:109], v190 offset:43520
	s_waitcnt lgkmcnt(13)
	v_mfma_f32_32x32x16_bf16 v[114:129], v[74:77], v[134:137], v[114:129]
	v_add_f32_e32 v74, v84, v138
	v_add_f32_e32 v74, v85, v74
	v_add_f32_e32 v74, v86, v74
	v_add_f32_e32 v110, v87, v74
	v_cvt_pk_bf16_f32 v142, v82, v83
	v_cvt_pk_bf16_f32 v143, v84, v85
	ds_read_b64_tr_b16 v[74:75], v190 offset:47104
	ds_read_b64_tr_b16 v[76:77], v190 offset:47616
	s_waitcnt lgkmcnt(14)
	v_mfma_f32_32x32x16_bf16 v[50:65], v[170:173], v[134:137], v[50:65]
	v_add_f32_e32 v82, v88, v110
	v_add_f32_e32 v82, v89, v82
	v_add_f32_e32 v82, v90, v82
	v_add_f32_e32 v82, v91, v82
	v_cvt_pk_bf16_f32 v144, v86, v87
	v_cvt_pk_bf16_f32 v145, v88, v89
	ds_read_b64_tr_b16 v[86:87], v190 offset:44032
	ds_read_b64_tr_b16 v[88:89], v190 offset:44544
	s_waitcnt lgkmcnt(14)
	v_mfma_f32_32x32x16_bf16 v[114:129], v[78:81], v[130:133], v[114:129]
	v_add_f32_e32 v78, v92, v82
	v_add_f32_e32 v78, v93, v78
	v_add_f32_e32 v78, v94, v78
	v_add_f32_e32 v82, v95, v78
	v_cvt_pk_bf16_f32 v138, v90, v91
	v_cvt_pk_bf16_f32 v139, v92, v93
	ds_read_b64_tr_b16 v[78:79], v190 offset:48128
	ds_read_b64_tr_b16 v[80:81], v190 offset:48640
	v_mfma_f32_32x32x16_bf16 v[50:65], v[66:69], v[130:133], v[50:65]
	v_add_f32_e32 v66, v96, v82
	v_add_f32_e32 v66, v97, v66
	v_add_f32_e32 v66, 0, v66
	v_cvt_pk_bf16_f32 v140, v94, v95
	v_cvt_pk_bf16_f32 v141, v96, v97
	s_mov_b64 s[42:43], 0x1f8000
	v_add_f32_e32 v179, v179, v66
	v_lshl_add_u64 v[66:67], v[176:177], 0, s[42:43]
	s_mov_b32 s3, m0
	s_mov_b32 m0, s27
	s_nop 0
	global_load_lds_dwordx4 v[66:67], off
	s_mov_b32 m0, s3
	s_mov_b64 s[28:29], 0x1e8000
	v_lshl_add_u64 v[66:67], v[174:175], 0, s[28:29]
	s_add_i32 s3, s2, 0x8000
	s_mov_b32 s23, m0
	s_mov_b32 m0, s3
	s_nop 0
	global_load_lds_dwordx4 v[66:67], off
	s_mov_b32 m0, s23
	s_waitcnt lgkmcnt(14)
	v_mfma_f32_32x32x16_bf16 v[2:17], v[158:161], v[192:195], v[2:17]
	v_exp_f32_e32 v114, v114
	v_exp_f32_e32 v115, v115
	v_exp_f32_e32 v116, v116
	v_exp_f32_e32 v117, v117
	s_waitcnt lgkmcnt(12)
	v_mfma_f32_32x32x16_bf16 v[18:33], v[158:161], v[98:101], v[18:33]
	v_exp_f32_e32 v118, v118
	v_exp_f32_e32 v119, v119
	v_exp_f32_e32 v120, v120
	v_exp_f32_e32 v121, v121
	ds_read_b128 v[66:69], v191 offset:8192
	ds_read_b128 v[90:93], v191 offset:8704
	s_waitcnt lgkmcnt(12)
; #define WAIT_BAR(N) asm volatile("s_waitcnt vmcnt(" #N ") lgkmcnt(0)\n\ts_barrier":::"memory")
;   #define RESC() do{ if(resc){ asm volatile("s_waitcnt lgkmcnt(0)":::"memory"); \
;       _Pragma("unroll") for(int d_=0;d_<2;++d_) _Pragma("unroll") for(int r=0;r<16;++r)o[d_][r]*=wsf[crow(r,hi)]; } }while(0)
;   #define ROT() do{sl_prev=sl_cur;sl_cur=sl_next;sl_next=(sl_next==(NSLOT-1)*SLOTB)?0:sl_next+SLOTB;}while(0)
;   #define ENDW(tt) do{ if((tt)+3<NT){WAIT_BAR(2);} else if((tt)+2<NT){WAIT_BAR(1);} else {WAIT_BAR(0);} }while(0)
;     ...
;   int t=1;
;     ...
;   for(;t+5<NT;t+=2){
;     STEP(pB0,pB1,pA0,pA1,t,true,true,true);     WAIT_BAR(2); RESC(); ROT();
;     STEP(pA0,pA1,pB0,pB1,t+1,true,true,true);   WAIT_BAR(2); RESC(); ROT();
;   }
;     ...
;   for(;t+1<NT;t+=2){
;     STEP(pB0,pB1,pA0,pA1,t,(t+3<NT),(t+1<NT),(t+1<NT));       ENDW(t);   RESC(); ROT();
;     STEP(pA0,pA1,pB0,pB1,t+1,(t+4<NT),(t+2<NT),(t+2<NT));     ENDW(t+1); RESC(); ROT();
	v_mfma_f32_32x32x16_bf16 v[2:17], v[150:153], v[102:105], v[2:17]
	v_exp_f32_e32 v122, v122
	v_exp_f32_e32 v123, v123
	v_exp_f32_e32 v124, v124
	v_exp_f32_e32 v125, v125
	ds_read_b128 v[94:97], v191 offset:10240
	ds_read_b128 v[162:165], v191 offset:10752
	s_waitcnt lgkmcnt(12)
	v_mfma_f32_32x32x16_bf16 v[18:33], v[150:153], v[70:73], v[18:33]
	v_exp_f32_e32 v126, v126
	v_exp_f32_e32 v127, v127
	v_exp_f32_e32 v128, v128
	v_exp_f32_e32 v129, v129
	ds_read_b128 v[166:169], v191 offset:12288
	ds_read_b128 v[170:173], v191 offset:12800
	s_waitcnt lgkmcnt(12)
	v_mfma_f32_32x32x16_bf16 v[2:17], v[142:145], v[106:109], v[2:17]
	v_exp_f32_e32 v50, v50
	v_exp_f32_e32 v51, v51
	v_exp_f32_e32 v52, v52
	v_exp_f32_e32 v53, v53
	ds_read_b128 v[192:195], v191 offset:14336
	ds_read_b128 v[82:85], v191 offset:14848
	s_waitcnt lgkmcnt(12)
	v_mfma_f32_32x32x16_bf16 v[18:33], v[142:145], v[74:77], v[18:33]
	v_exp_f32_e32 v54, v54
	v_exp_f32_e32 v55, v55
	v_exp_f32_e32 v56, v56
	v_exp_f32_e32 v57, v57
	s_waitcnt lgkmcnt(10)
	v_mfma_f32_32x32x16_bf16 v[2:17], v[138:141], v[86:89], v[2:17]
	v_exp_f32_e32 v58, v58
	v_exp_f32_e32 v59, v59
	v_exp_f32_e32 v60, v60
	v_exp_f32_e32 v61, v61
	s_waitcnt lgkmcnt(8)
	v_mfma_f32_32x32x16_bf16 v[18:33], v[138:141], v[78:81], v[18:33]
	v_exp_f32_e32 v62, v62
	v_exp_f32_e32 v63, v63
	v_exp_f32_e32 v64, v64
	v_exp_f32_e32 v65, v65
	s_waitcnt vmcnt(2) lgkmcnt(0)
	s_barrier
	ds_read_b64_tr_b16 v[86:87], v190 offset:24576
	ds_read_b64_tr_b16 v[88:89], v190 offset:25088
	v_add_f32_e32 v70, v114, v115
	v_add_f32_e32 v70, v116, v70
	v_add_f32_e32 v70, v117, v70
	v_add_f32_e32 v70, v118, v70
	v_add_f32_e32 v70, v119, v70
	v_cvt_pk_bf16_f32 v158, v114, v115
	v_cvt_pk_bf16_f32 v159, v116, v117
	s_waitcnt lgkmcnt(9)
	v_mfma_f32_32x32x16_bf16 v[98:113], v[66:69], v[154:157], v[34:49]
	ds_read_b64_tr_b16 v[114:115], v190 offset:28672
	ds_read_b64_tr_b16 v[116:117], v190 offset:29184
	v_add_f32_e32 v66, v120, v70
	v_add_f32_e32 v66, v121, v66
	v_add_f32_e32 v66, v122, v66
	v_add_f32_e32 v138, v123, v66
	v_cvt_pk_bf16_f32 v160, v118, v119
	v_cvt_pk_bf16_f32 v161, v120, v121
	s_waitcnt lgkmcnt(10)
	v_mfma_f32_32x32x16_bf16 v[66:81], v[90:93], v[154:157], v[34:49]
	ds_read_b64_tr_b16 v[90:91], v190 offset:25600
	ds_read_b64_tr_b16 v[92:93], v190 offset:26112
	s_waitcnt lgkmcnt(11)
	v_mfma_f32_32x32x16_bf16 v[98:113], v[94:97], v[146:149], v[98:113]
	v_add_f32_e32 v94, v124, v138
	v_add_f32_e32 v94, v125, v94
	v_add_f32_e32 v94, v126, v94
	v_add_f32_e32 v118, v127, v94
	v_cvt_pk_bf16_f32 v150, v122, v123
	v_cvt_pk_bf16_f32 v151, v124, v125
	ds_read_b64_tr_b16 v[94:95], v190 offset:29696
	ds_read_b64_tr_b16 v[96:97], v190 offset:30208
	v_add_f32_e32 v118, v128, v118
	v_add_f32_e32 v118, v129, v118
	v_add_f32_e32 v118, v50, v118
	v_add_f32_e32 v122, v51, v118
	v_cvt_pk_bf16_f32 v152, v126, v127
	v_cvt_pk_bf16_f32 v153, v128, v129
	s_waitcnt lgkmcnt(12)
	v_mfma_f32_32x32x16_bf16 v[66:81], v[162:165], v[146:149], v[66:81]
	ds_read_b64_tr_b16 v[118:119], v190 offset:26624
	ds_read_b64_tr_b16 v[120:121], v190 offset:27136
	v_add_f32_e32 v122, v52, v122
	v_add_f32_e32 v122, v53, v122
	v_add_f32_e32 v122, v54, v122
	v_add_f32_e32 v122, v55, v122
	v_cvt_pk_bf16_f32 v142, v50, v51
	v_cvt_pk_bf16_f32 v143, v52, v53
	s_waitcnt lgkmcnt(13)
	v_mfma_f32_32x32x16_bf16 v[98:113], v[166:169], v[134:137], v[98:113]
	ds_read_b64_tr_b16 v[50:51], v190 offset:30720
	ds_read_b64_tr_b16 v[52:53], v190 offset:31232
	v_add_f32_e32 v122, v56, v122
	v_add_f32_e32 v122, v57, v122
	v_add_f32_e32 v122, v58, v122
	v_add_f32_e32 v122, v59, v122
	v_cvt_pk_bf16_f32 v144, v54, v55
	v_cvt_pk_bf16_f32 v145, v56, v57
	s_waitcnt lgkmcnt(14)
	v_mfma_f32_32x32x16_bf16 v[66:81], v[170:173], v[134:137], v[66:81]
	ds_read_b64_tr_b16 v[54:55], v190 offset:27648
	ds_read_b64_tr_b16 v[56:57], v190 offset:28160
	v_add_f32_e32 v122, v60, v122
	v_add_f32_e32 v122, v61, v122
	v_add_f32_e32 v122, v62, v122
	v_add_f32_e32 v122, v63, v122
	v_cvt_pk_bf16_f32 v138, v58, v59
	v_cvt_pk_bf16_f32 v139, v60, v61
	s_waitcnt lgkmcnt(14)
	v_mfma_f32_32x32x16_bf16 v[98:113], v[192:195], v[130:133], v[98:113]
	ds_read_b64_tr_b16 v[58:59], v190 offset:31744
	ds_read_b64_tr_b16 v[60:61], v190 offset:32256
	v_mfma_f32_32x32x16_bf16 v[66:81], v[82:85], v[130:133], v[66:81]
	v_add_f32_e32 v82, v64, v122
	v_add_f32_e32 v82, v65, v82
	v_add_f32_e32 v82, 0, v82
	v_cvt_pk_bf16_f32 v140, v62, v63
	v_cvt_pk_bf16_f32 v141, v64, v65
	v_lshl_add_u64 v[62:63], v[174:175], 0, s[30:31]
	s_add_i32 s2, s2, 0xa000
	s_mov_b32 s3, m0
	s_mov_b32 m0, s2
	s_nop 0
	global_load_lds_dwordx4 v[62:63], off
	s_mov_b32 m0, s3
	v_add_f32_e32 v176, v179, v82
	s_waitcnt lgkmcnt(14)
	v_mfma_f32_32x32x16_bf16 v[2:17], v[158:161], v[86:89], v[2:17]
	v_exp_f32_e32 v98, v98
	v_exp_f32_e32 v99, v99
	v_exp_f32_e32 v100, v100
	v_exp_f32_e32 v101, v101
	s_waitcnt lgkmcnt(12)
	v_mfma_f32_32x32x16_bf16 v[18:33], v[158:161], v[114:117], v[18:33]
	v_exp_f32_e32 v102, v102
	v_exp_f32_e32 v103, v103
	v_exp_f32_e32 v104, v104
	v_exp_f32_e32 v105, v105
	ds_read_b128 v[62:65], v191 offset:16384
	ds_read_b128 v[122:125], v191 offset:16896
	s_waitcnt lgkmcnt(12)
	v_mfma_f32_32x32x16_bf16 v[2:17], v[150:153], v[90:93], v[2:17]
	v_exp_f32_e32 v106, v106
	v_exp_f32_e32 v107, v107
	v_exp_f32_e32 v108, v108
	v_exp_f32_e32 v109, v109
	ds_read_b128 v[126:129], v191 offset:18432
	ds_read_b128 v[162:165], v191 offset:18944
	s_waitcnt lgkmcnt(12)
	v_mfma_f32_32x32x16_bf16 v[18:33], v[150:153], v[94:97], v[18:33]
	v_exp_f32_e32 v110, v110
	v_exp_f32_e32 v111, v111
	v_exp_f32_e32 v112, v112
	v_exp_f32_e32 v113, v113
	ds_read_b128 v[166:169], v191 offset:20480
	ds_read_b128 v[170:173], v191 offset:20992
	s_waitcnt lgkmcnt(12)
	v_mfma_f32_32x32x16_bf16 v[2:17], v[142:145], v[118:121], v[2:17]
	v_exp_f32_e32 v66, v66
	v_exp_f32_e32 v67, v67
	v_exp_f32_e32 v68, v68
	v_exp_f32_e32 v69, v69
	ds_read_b128 v[118:121], v191 offset:22528
	ds_read_b128 v[114:117], v191 offset:23040
	s_waitcnt lgkmcnt(12)
	v_mfma_f32_32x32x16_bf16 v[18:33], v[142:145], v[50:53], v[18:33]
	v_exp_f32_e32 v70, v70
	v_exp_f32_e32 v71, v71
	v_exp_f32_e32 v72, v72
	v_exp_f32_e32 v73, v73
	s_waitcnt lgkmcnt(10)
	v_mfma_f32_32x32x16_bf16 v[2:17], v[138:141], v[54:57], v[2:17]
	v_exp_f32_e32 v74, v74
	v_exp_f32_e32 v75, v75
	v_exp_f32_e32 v76, v76
	v_exp_f32_e32 v77, v77
	s_waitcnt lgkmcnt(8)
	v_mfma_f32_32x32x16_bf16 v[18:33], v[138:141], v[58:61], v[18:33]
	v_exp_f32_e32 v78, v78
	v_exp_f32_e32 v79, v79
	v_exp_f32_e32 v80, v80
	v_exp_f32_e32 v81, v81
	s_waitcnt vmcnt(1) lgkmcnt(0)
	s_barrier
; #define WAIT_BAR(N) asm volatile("s_waitcnt vmcnt(" #N ") lgkmcnt(0)\n\ts_barrier":::"memory")
;   #define RESC() do{ if(resc){ asm volatile("s_waitcnt lgkmcnt(0)":::"memory"); \
;       _Pragma("unroll") for(int d_=0;d_<2;++d_) _Pragma("unroll") for(int r=0;r<16;++r)o[d_][r]*=wsf[crow(r,hi)]; } }while(0)
;   #define ROT() do{sl_prev=sl_cur;sl_cur=sl_next;sl_next=(sl_next==(NSLOT-1)*SLOTB)?0:sl_next+SLOTB;}while(0)
;   #define ENDW(tt) do{ if((tt)+3<NT){WAIT_BAR(2);} else if((tt)+2<NT){WAIT_BAR(1);} else {WAIT_BAR(0);} }while(0)
;     ...
;   int t=1;
;     ...
;   for(;t+5<NT;t+=2){
;     STEP(pB0,pB1,pA0,pA1,t,true,true,true);     WAIT_BAR(2); RESC(); ROT();
;     STEP(pA0,pA1,pB0,pB1,t+1,true,true,true);   WAIT_BAR(2); RESC(); ROT();
;   }
;     ...
;   for(;t+1<NT;t+=2){
;     STEP(pB0,pB1,pA0,pA1,t,(t+3<NT),(t+1<NT),(t+1<NT));       ENDW(t);   RESC(); ROT();
;     STEP(pA0,pA1,pB0,pB1,t+1,(t+4<NT),(t+2<NT),(t+2<NT));     ENDW(t+1); RESC(); ROT();
	ds_read_b64_tr_b16 v[192:193], v190 offset:32768
	ds_read_b64_tr_b16 v[194:195], v190 offset:33280
	v_add_f32_e32 v50, v98, v99
	v_add_f32_e32 v50, v100, v50
	v_add_f32_e32 v50, v101, v50
	v_add_f32_e32 v50, v102, v50
	v_add_f32_e32 v50, v103, v50
	v_cvt_pk_bf16_f32 v158, v98, v99
	v_cvt_pk_bf16_f32 v159, v100, v101
	s_waitcnt lgkmcnt(9)
	v_mfma_f32_32x32x16_bf16 v[82:97], v[62:65], v[154:157], v[34:49]
	ds_read_b64_tr_b16 v[98:99], v190 offset:36864
	ds_read_b64_tr_b16 v[100:101], v190 offset:37376
	v_add_f32_e32 v50, v104, v50
	v_add_f32_e32 v50, v105, v50
	v_add_f32_e32 v50, v106, v50
	v_add_f32_e32 v138, v107, v50
	s_waitcnt lgkmcnt(10)
	v_mfma_f32_32x32x16_bf16 v[50:65], v[122:125], v[154:157], v[34:49]
	v_cvt_pk_bf16_f32 v160, v102, v103
	v_cvt_pk_bf16_f32 v161, v104, v105
	ds_read_b64_tr_b16 v[122:123], v190 offset:33792
	ds_read_b64_tr_b16 v[124:125], v190 offset:34304
	v_add_f32_e32 v102, v108, v138
	v_add_f32_e32 v102, v109, v102
	v_add_f32_e32 v102, v110, v102
	v_add_f32_e32 v102, v111, v102
	v_cvt_pk_bf16_f32 v150, v106, v107
	v_cvt_pk_bf16_f32 v151, v108, v109
	s_waitcnt lgkmcnt(11)
	v_mfma_f32_32x32x16_bf16 v[82:97], v[126:129], v[146:149], v[82:97]
	ds_read_b64_tr_b16 v[104:105], v190 offset:37888
	ds_read_b64_tr_b16 v[106:107], v190 offset:38400
	s_waitcnt lgkmcnt(12)
	v_mfma_f32_32x32x16_bf16 v[50:65], v[162:165], v[146:149], v[50:65]
	v_add_f32_e32 v102, v112, v102
	v_add_f32_e32 v102, v113, v102
	v_add_f32_e32 v102, v66, v102
	v_add_f32_e32 v102, v67, v102
	v_cvt_pk_bf16_f32 v152, v110, v111
	v_cvt_pk_bf16_f32 v153, v112, v113
	ds_read_b64_tr_b16 v[108:109], v190 offset:34816
	ds_read_b64_tr_b16 v[110:111], v190 offset:35328
	v_add_f32_e32 v102, v68, v102
	v_add_f32_e32 v102, v69, v102
	v_add_f32_e32 v102, v70, v102
	v_add_f32_e32 v102, v71, v102
	v_cvt_pk_bf16_f32 v142, v66, v67
	v_cvt_pk_bf16_f32 v143, v68, v69
	s_waitcnt lgkmcnt(13)
	v_mfma_f32_32x32x16_bf16 v[82:97], v[166:169], v[134:137], v[82:97]
	ds_read_b64_tr_b16 v[66:67], v190 offset:38912
	ds_read_b64_tr_b16 v[68:69], v190 offset:39424
	s_waitcnt lgkmcnt(14)
	v_mfma_f32_32x32x16_bf16 v[50:65], v[170:173], v[134:137], v[50:65]
	v_add_f32_e32 v102, v72, v102
	v_add_f32_e32 v102, v73, v102
	v_add_f32_e32 v102, v74, v102
	v_add_f32_e32 v102, v75, v102
	v_cvt_pk_bf16_f32 v144, v70, v71
	v_cvt_pk_bf16_f32 v145, v72, v73
	ds_read_b64_tr_b16 v[70:71], v190 offset:35840
	ds_read_b64_tr_b16 v[72:73], v190 offset:36352
	v_add_f32_e32 v102, v76, v102
	v_add_f32_e32 v102, v77, v102
	v_add_f32_e32 v102, v78, v102
	v_add_f32_e32 v102, v79, v102
	v_cvt_pk_bf16_f32 v138, v74, v75
	v_cvt_pk_bf16_f32 v139, v76, v77
	s_waitcnt lgkmcnt(14)
	v_mfma_f32_32x32x16_bf16 v[82:97], v[118:121], v[130:133], v[82:97]
	ds_read_b64_tr_b16 v[74:75], v190 offset:39936
	ds_read_b64_tr_b16 v[76:77], v190 offset:40448
	v_mfma_f32_32x32x16_bf16 v[50:65], v[114:117], v[130:133], v[50:65]
	v_add_f32_e32 v102, v80, v102
	v_add_f32_e32 v102, v81, v102
	v_add_f32_e32 v102, 0, v102
	v_cvt_pk_bf16_f32 v140, v78, v79
	v_cvt_pk_bf16_f32 v141, v80, v81
	v_lshl_add_u64 v[78:79], v[174:175], 0, s[42:43]
	s_mov_b32 s2, m0
	s_mov_b32 m0, s26
	s_nop 0
	global_load_lds_dwordx4 v[78:79], off
	s_mov_b32 m0, s2
	v_add_f32_e32 v102, v176, v102
	s_waitcnt lgkmcnt(14)
	v_mfma_f32_32x32x16_bf16 v[2:17], v[158:161], v[192:195], v[2:17]
	v_exp_f32_e32 v82, v82
	v_exp_f32_e32 v83, v83
	v_exp_f32_e32 v84, v84
	v_exp_f32_e32 v85, v85
	s_waitcnt lgkmcnt(12)
	v_mfma_f32_32x32x16_bf16 v[18:33], v[158:161], v[98:101], v[18:33]
	v_exp_f32_e32 v86, v86
	v_exp_f32_e32 v87, v87
	v_exp_f32_e32 v88, v88
	v_exp_f32_e32 v89, v89
	ds_read_b128 v[112:115], v191
	ds_read_b128 v[116:119], v191 offset:512
	s_waitcnt lgkmcnt(12)
	v_mfma_f32_32x32x16_bf16 v[2:17], v[150:153], v[122:125], v[2:17]
	v_exp_f32_e32 v90, v90
	v_exp_f32_e32 v91, v91
	v_exp_f32_e32 v92, v92
	v_exp_f32_e32 v93, v93
	ds_read_b128 v[120:123], v191 offset:2048
	ds_read_b128 v[124:127], v191 offset:2560
	s_waitcnt lgkmcnt(12)
	v_mfma_f32_32x32x16_bf16 v[18:33], v[150:153], v[104:107], v[18:33]
	v_exp_f32_e32 v94, v94
	v_exp_f32_e32 v95, v95
	v_exp_f32_e32 v96, v96
	v_exp_f32_e32 v97, v97
	ds_read_b128 v[104:107], v191 offset:4096
	ds_read_b128 v[162:165], v191 offset:4608
	s_waitcnt lgkmcnt(12)
	v_mfma_f32_32x32x16_bf16 v[2:17], v[142:145], v[108:111], v[2:17]
	v_exp_f32_e32 v50, v50
	v_exp_f32_e32 v51, v51
	v_exp_f32_e32 v52, v52
	v_exp_f32_e32 v53, v53
	ds_read_b128 v[108:111], v191 offset:6144
	ds_read_b128 v[98:101], v191 offset:6656
	s_waitcnt lgkmcnt(12)
	v_mfma_f32_32x32x16_bf16 v[18:33], v[142:145], v[66:69], v[18:33]
	v_exp_f32_e32 v54, v54
	v_exp_f32_e32 v55, v55
	v_exp_f32_e32 v56, v56
	v_exp_f32_e32 v57, v57
	s_waitcnt lgkmcnt(10)
	v_mfma_f32_32x32x16_bf16 v[2:17], v[138:141], v[70:73], v[2:17]
	v_exp_f32_e32 v58, v58
	v_exp_f32_e32 v59, v59
	v_exp_f32_e32 v60, v60
	v_exp_f32_e32 v61, v61
	s_waitcnt lgkmcnt(8)
	v_mfma_f32_32x32x16_bf16 v[18:33], v[138:141], v[74:77], v[18:33]
	v_exp_f32_e32 v62, v62
	v_exp_f32_e32 v63, v63
	v_exp_f32_e32 v64, v64
	v_exp_f32_e32 v65, v65
	s_waitcnt vmcnt(0) lgkmcnt(0)
	s_barrier
; #define SBAR() __builtin_amdgcn_sched_barrier(0)
;   #define RESC() do{ if(resc){ asm volatile("s_waitcnt lgkmcnt(0)":::"memory"); \
;       _Pragma("unroll") for(int d_=0;d_<2;++d_) _Pragma("unroll") for(int r=0;r<16;++r)o[d_][r]*=wsf[crow(r,hi)]; } }while(0)
;   #define PKW(P,B) cvtpk_s(P[B],P[B+1])
; __device__ __forceinline__ void pv(f32x16*o,int vb,bf16x8 pa0,bf16x8 pa1,bf16x8 pa2,bf16x8 pa3){
;   #pragma unroll
;   for(int d0=0;d0<2;++d0){s16x4 lo[4],hi[4];
;     #pragma unroll
;     for(int ks=0;ks<4;++ks){
;       asm volatile("ds_read_b64_tr_b16 %0,%1 offset:%c2":"=&v"(lo[ks]):"v"(vb),"i"(d0*4096+ks*1024):"memory");
;       asm volatile("ds_read_b64_tr_b16 %0,%1 offset:%c2":"=&v"(hi[ks]):"v"(vb),"i"(d0*4096+ks*1024+512):"memory");}
;     asm volatile("s_waitcnt lgkmcnt(0)":::"memory");SBAR();
;     ...
;     o[d0]=__builtin_amdgcn_mfma_f32_32x32x16_bf16(pa0,PK(0),o[d0],0,0,0);
;     o[d0]=__builtin_amdgcn_mfma_f32_32x32x16_bf16(pa1,PK(1),o[d0],0,0,0);
;     o[d0]=__builtin_amdgcn_mfma_f32_32x32x16_bf16(pa2,PK(2),o[d0],0,0,0);
;     o[d0]=__builtin_amdgcn_mfma_f32_32x32x16_bf16(pa3,PK(3),o[d0],0,0,0);
;     ...
;   }
; }
;     ...
;   STEP(pB0,pB1,pA0,pA1,NT-1,false,false,false); RESC();
;   { float sacc=pB0[0]+pB0[1]; _Pragma("unroll") for(int r=2;r<16;++r)sacc+=pB0[r]; _Pragma("unroll") for(int r=0;r<16;++r)sacc+=pB1[r]; l_reg+=sacc;
;     pw0=(u32x4){PKW(pB0,0),PKW(pB0,2),PKW(pB0,4),PKW(pB0,6)};pw1=(u32x4){PKW(pB0,8),PKW(pB0,10),PKW(pB0,12),PKW(pB0,14)};pw2=(u32x4){PKW(pB1,0),PKW(pB1,2),PKW(pB1,4),PKW(pB1,6)};pw3=(u32x4){PKW(pB1,8),PKW(pB1,10),PKW(pB1,12),PKW(pB1,14)};
;     SBAR(); pv(o,vb0+sl_cur,PAF(0),PAF(1),PAF(2),PAF(3)); }
	ds_read_b64_tr_b16 v[166:167], v190 offset:40960
	ds_read_b64_tr_b16 v[168:169], v190 offset:41472
	v_add_f32_e32 v66, v82, v83
	v_add_f32_e32 v66, v84, v66
	v_add_f32_e32 v66, v85, v66
	v_add_f32_e32 v66, v86, v66
	v_add_f32_e32 v103, v87, v66
	v_cvt_pk_bf16_f32 v158, v82, v83
	v_cvt_pk_bf16_f32 v159, v84, v85
	s_waitcnt lgkmcnt(9)
	v_mfma_f32_32x32x16_bf16 v[66:81], v[112:115], v[154:157], v[34:49]
	ds_read_b64_tr_b16 v[82:83], v190 offset:45056
	ds_read_b64_tr_b16 v[84:85], v190 offset:45568
	s_waitcnt lgkmcnt(10)
	v_mfma_f32_32x32x16_bf16 v[34:49], v[116:119], v[154:157], v[34:49]
	v_add_f32_e32 v103, v88, v103
	v_add_f32_e32 v103, v89, v103
	v_add_f32_e32 v103, v90, v103
	v_add_f32_e32 v103, v91, v103
	v_cvt_pk_bf16_f32 v160, v86, v87
	v_cvt_pk_bf16_f32 v161, v88, v89
	ds_read_b64_tr_b16 v[86:87], v190 offset:41984
	ds_read_b64_tr_b16 v[88:89], v190 offset:42496
	v_add_f32_e32 v103, v92, v103
	v_add_f32_e32 v103, v93, v103
	v_add_f32_e32 v103, v94, v103
	v_add_f32_e32 v103, v95, v103
	v_cvt_pk_bf16_f32 v150, v90, v91
	v_cvt_pk_bf16_f32 v151, v92, v93
	s_waitcnt lgkmcnt(11)
	v_mfma_f32_32x32x16_bf16 v[66:81], v[120:123], v[146:149], v[66:81]
	ds_read_b64_tr_b16 v[90:91], v190 offset:46080
	ds_read_b64_tr_b16 v[92:93], v190 offset:46592
	s_waitcnt lgkmcnt(12)
	v_mfma_f32_32x32x16_bf16 v[34:49], v[124:127], v[146:149], v[34:49]
	v_add_f32_e32 v103, v96, v103
	v_add_f32_e32 v103, v97, v103
	v_add_f32_e32 v103, v50, v103
	v_add_f32_e32 v103, v51, v103
	v_cvt_pk_bf16_f32 v152, v94, v95
	v_cvt_pk_bf16_f32 v153, v96, v97
	ds_read_b64_tr_b16 v[94:95], v190 offset:43008
	ds_read_b64_tr_b16 v[96:97], v190 offset:43520
	v_add_f32_e32 v103, v52, v103
	v_add_f32_e32 v103, v53, v103
	v_add_f32_e32 v103, v54, v103
	v_add_f32_e32 v103, v55, v103
	v_cvt_pk_bf16_f32 v142, v50, v51
	v_cvt_pk_bf16_f32 v143, v52, v53
	s_waitcnt lgkmcnt(13)
	v_mfma_f32_32x32x16_bf16 v[66:81], v[104:107], v[134:137], v[66:81]
	ds_read_b64_tr_b16 v[50:51], v190 offset:47104
	ds_read_b64_tr_b16 v[52:53], v190 offset:47616
	s_waitcnt lgkmcnt(14)
	v_mfma_f32_32x32x16_bf16 v[34:49], v[162:165], v[134:137], v[34:49]
	v_add_f32_e32 v103, v56, v103
	v_add_f32_e32 v103, v57, v103
	v_add_f32_e32 v103, v58, v103
	v_add_f32_e32 v103, v59, v103
	v_cvt_pk_bf16_f32 v144, v54, v55
	v_cvt_pk_bf16_f32 v145, v56, v57
	ds_read_b64_tr_b16 v[54:55], v190 offset:44032
	ds_read_b64_tr_b16 v[56:57], v190 offset:44544
	v_add_f32_e32 v103, v60, v103
	v_add_f32_e32 v103, v61, v103
	v_add_f32_e32 v103, v62, v103
	v_add_f32_e32 v103, v63, v103
	v_cvt_pk_bf16_f32 v138, v58, v59
	v_cvt_pk_bf16_f32 v139, v60, v61
	s_waitcnt lgkmcnt(14)
	v_mfma_f32_32x32x16_bf16 v[66:81], v[108:111], v[130:133], v[66:81]
	ds_read_b64_tr_b16 v[58:59], v190 offset:48128
	ds_read_b64_tr_b16 v[60:61], v190 offset:48640
	v_mfma_f32_32x32x16_bf16 v[34:49], v[98:101], v[130:133], v[34:49]
	v_add_f32_e32 v98, v64, v103
	v_add_f32_e32 v98, v65, v98
	v_add_f32_e32 v98, 0, v98
	v_cvt_pk_bf16_f32 v140, v62, v63
	v_cvt_pk_bf16_f32 v141, v64, v65
	s_waitcnt lgkmcnt(14)
	v_mfma_f32_32x32x16_bf16 v[2:17], v[158:161], v[166:169], v[2:17]
	s_nop 1
	v_exp_f32_e32 v66, v66
	v_exp_f32_e32 v67, v67
	v_exp_f32_e32 v68, v68
	v_exp_f32_e32 v69, v69
	s_waitcnt lgkmcnt(12)
	v_mfma_f32_32x32x16_bf16 v[18:33], v[158:161], v[82:85], v[18:33]
	v_exp_f32_e32 v70, v70
	v_exp_f32_e32 v71, v71
	v_exp_f32_e32 v72, v72
	v_exp_f32_e32 v73, v73
	s_waitcnt lgkmcnt(10)
	v_mfma_f32_32x32x16_bf16 v[2:17], v[150:153], v[86:89], v[2:17]
	v_exp_f32_e32 v74, v74
	v_exp_f32_e32 v75, v75
	v_exp_f32_e32 v76, v76
	v_exp_f32_e32 v77, v77
	s_waitcnt lgkmcnt(8)
	v_mfma_f32_32x32x16_bf16 v[18:33], v[150:153], v[90:93], v[18:33]
	v_exp_f32_e32 v78, v78
	v_exp_f32_e32 v79, v79
	v_exp_f32_e32 v80, v80
	v_exp_f32_e32 v81, v81
	s_waitcnt lgkmcnt(6)
	v_mfma_f32_32x32x16_bf16 v[2:17], v[142:145], v[94:97], v[2:17]
	v_exp_f32_e32 v34, v34
	v_exp_f32_e32 v35, v35
	v_exp_f32_e32 v36, v36
	v_exp_f32_e32 v37, v37
	s_waitcnt lgkmcnt(4)
	v_mfma_f32_32x32x16_bf16 v[18:33], v[142:145], v[50:53], v[18:33]
	v_exp_f32_e32 v38, v38
	v_exp_f32_e32 v39, v39
	v_exp_f32_e32 v40, v40
	v_exp_f32_e32 v41, v41
	s_waitcnt lgkmcnt(2)
	v_mfma_f32_32x32x16_bf16 v[2:17], v[138:141], v[54:57], v[2:17]
	v_exp_f32_e32 v42, v42
	v_exp_f32_e32 v43, v43
	v_exp_f32_e32 v44, v44
	v_exp_f32_e32 v45, v45
	s_waitcnt lgkmcnt(0)
	v_mfma_f32_32x32x16_bf16 v[18:33], v[138:141], v[58:61], v[18:33]
	v_exp_f32_e32 v46, v46
	v_exp_f32_e32 v47, v47
	v_exp_f32_e32 v48, v48
	v_exp_f32_e32 v49, v49
	v_add_f32_e32 v50, v66, v67
	v_add_f32_e32 v50, v68, v50
	v_add_f32_e32 v50, v69, v50
	v_add_f32_e32 v50, v70, v50
	v_add_f32_e32 v50, v71, v50
	v_add_f32_e32 v50, v72, v50
	v_add_f32_e32 v50, v73, v50
	v_add_f32_e32 v50, v74, v50
	v_add_f32_e32 v50, v75, v50
	v_add_f32_e32 v50, v76, v50
	v_add_f32_e32 v50, v77, v50
	v_add_f32_e32 v50, v78, v50
	v_add_f32_e32 v50, v79, v50
	v_add_f32_e32 v50, v80, v50
	v_add_f32_e32 v50, v81, v50
	v_add_f32_e32 v50, v34, v50
	v_add_f32_e32 v50, v35, v50
	v_add_f32_e32 v50, v36, v50
	v_add_f32_e32 v50, v37, v50
	v_add_f32_e32 v50, v38, v50
	v_add_f32_e32 v50, v39, v50
	v_add_f32_e32 v50, v40, v50
	v_add_f32_e32 v50, v41, v50
	v_add_f32_e32 v50, v42, v50
	v_add_f32_e32 v50, v43, v50
	v_add_f32_e32 v50, v44, v50
	v_add_f32_e32 v50, v45, v50
	v_add_f32_e32 v50, v46, v50
	v_add_f32_e32 v50, v47, v50
	v_add_f32_e32 v50, v48, v50
	v_add_f32_e32 v50, v49, v50
	v_add_f32_e32 v51, v102, v98
	v_add_f32_e32 v50, v51, v50
	v_cvt_pk_bf16_f32 v34, v34, v35
	v_cvt_pk_bf16_f32 v52, v66, v67
	v_cvt_pk_bf16_f32 v53, v68, v69
	v_cvt_pk_bf16_f32 v54, v70, v71
	v_cvt_pk_bf16_f32 v55, v72, v73
	v_cvt_pk_bf16_f32 v56, v74, v75
	v_cvt_pk_bf16_f32 v57, v76, v77
	v_cvt_pk_bf16_f32 v58, v78, v79
	v_cvt_pk_bf16_f32 v59, v80, v81
	v_cvt_pk_bf16_f32 v35, v36, v37
	v_cvt_pk_bf16_f32 v36, v38, v39
	v_cvt_pk_bf16_f32 v37, v40, v41
	v_cvt_pk_bf16_f32 v38, v42, v43
	v_cvt_pk_bf16_f32 v39, v44, v45
	v_cvt_pk_bf16_f32 v40, v46, v47
	v_cvt_pk_bf16_f32 v41, v48, v49
	ds_read_b64_tr_b16 v[42:43],v178 offset:0
	ds_read_b64_tr_b16 v[44:45],v178 offset:512
	ds_read_b64_tr_b16 v[46:47],v178 offset:1024
	ds_read_b64_tr_b16 v[48:49],v178 offset:1536
	ds_read_b64_tr_b16 v[60:61],v178 offset:2048
	ds_read_b64_tr_b16 v[62:63],v178 offset:2560
	ds_read_b64_tr_b16 v[64:65],v178 offset:3072
	ds_read_b64_tr_b16 v[66:67],v178 offset:3584
	s_waitcnt lgkmcnt(0)
; __device__ __forceinline__ int crow(int r,int hi){return (r&3)+8*(r>>2)+4*hi;}
; #define SBAR() __builtin_amdgcn_sched_barrier(0)
; __device__ __forceinline__ void pv(f32x16*o,int vb,bf16x8 pa0,bf16x8 pa1,bf16x8 pa2,bf16x8 pa3){
;     ...
;     asm volatile("s_waitcnt lgkmcnt(0)":::"memory");SBAR();
;     ...
;     o[d0]=__builtin_amdgcn_mfma_f32_32x32x16_bf16(pa0,PK(0),o[d0],0,0,0);
;     o[d0]=__builtin_amdgcn_mfma_f32_32x32x16_bf16(pa1,PK(1),o[d0],0,0,0);
;     o[d0]=__builtin_amdgcn_mfma_f32_32x32x16_bf16(pa2,PK(2),o[d0],0,0,0);
;     o[d0]=__builtin_amdgcn_mfma_f32_32x32x16_bf16(pa3,PK(3),o[d0],0,0,0);
;     ...
;   }
; }
;     ...
;   {auto rr=__builtin_amdgcn_permlane32_swap(__float_as_uint(l_reg),__float_as_uint(l_reg),false,false);l_reg=__uint_as_float(rr[0])+__uint_as_float(rr[1]);}
;   if(hi==0)wsf[32+r32]=l_reg;asm volatile("s_waitcnt lgkmcnt(0)":::"memory");
;   float rli[16];
;   #pragma unroll
;   for(int r=0;r<16;++r)rli[r]=__builtin_amdgcn_rcpf(wsf[32+crow(r,hi)]);
;   bf16*Ow=O+(rowbase+q0+wid*QBLK)*OP+h*D;
;   { bf16*stg=(bf16*)(shm+LDS_OST)+wid*2048;
;     #pragma unroll
;     for(int r=0;r<16;++r){const int orow=crow(r,hi);
;       #pragma unroll
;       for(int d0=0;d0<2;++d0)stg[orow*64+d0*32+r32]=__float2bfloat16(o[d0][r]*rli[r]);}
;     asm volatile("s_waitcnt lgkmcnt(0)":::"memory");
;     #pragma unroll
;     for(int i=0;i<4;++i){const int row=i*8+(lane>>3),ch=lane&7; const u32x4 v=*(const u32x4*)(stg+row*64+ch*8); ATTN_STORE16(Ow+(long)row*OP+ch*8,v);} }
;   asm volatile("s_waitcnt lgkmcnt(0)\n\ts_barrier":::"memory");
	s_nop 0
	v_mfma_f32_32x32x16_bf16 v[2:17], v[52:55], v[42:45], v[2:17]
	ds_read_b64_tr_b16 v[42:43],v178 offset:4096
	ds_read_b64_tr_b16 v[44:45],v178 offset:4608
	v_mfma_f32_32x32x16_bf16 v[2:17], v[56:59], v[46:49], v[2:17]
	ds_read_b64_tr_b16 v[46:47],v178 offset:5120
	ds_read_b64_tr_b16 v[48:49],v178 offset:5632
	v_mfma_f32_32x32x16_bf16 v[2:17], v[34:37], v[60:63], v[2:17]
	ds_read_b64_tr_b16 v[60:61],v178 offset:6144
	ds_read_b64_tr_b16 v[62:63],v178 offset:6656
	v_mfma_f32_32x32x16_bf16 v[2:17], v[38:41], v[64:67], v[2:17]
	ds_read_b64_tr_b16 v[64:65],v178 offset:7168
	ds_read_b64_tr_b16 v[66:67],v178 offset:7680
	s_waitcnt lgkmcnt(0)
	v_mfma_f32_32x32x16_bf16 v[18:33], v[52:55], v[42:45], v[18:33]
	v_cmp_gt_u32_e32 vcc, 32, v1
	v_mfma_f32_32x32x16_bf16 v[18:33], v[56:59], v[46:49], v[18:33]
	v_mfma_f32_32x32x16_bf16 v[18:33], v[34:37], v[60:63], v[18:33]
	v_mov_b32_e32 v34, v50
	s_nop 1
	v_permlane32_swap_b32_e32 v50, v34
	v_mfma_f32_32x32x16_bf16 v[18:33], v[38:41], v[64:67], v[18:33]
	s_and_saveexec_b64 s[2:3], vcc
	v_add_f32_e32 v34, v50, v34
	v_lshl_add_u32 v35, v188, 2, s22
	ds_write_b32 v35, v34 offset:49280
	s_or_b64 exec, exec, s[2:3]
	s_waitcnt lgkmcnt(0)
	v_lshl_add_u32 v42, v189, 4, s22
	ds_read_b128 v[34:37], v42 offset:49280
	ds_read_b128 v[38:41], v42 offset:49312
	s_lshl_b64 s[2:3], s[6:7], 11
	s_lshl_b32 s6, s25, 12
	s_add_i32 s6, s6, 0
	s_waitcnt lgkmcnt(1)
	v_rcp_f32_e32 v43, v34
	v_rcp_f32_e32 v44, v35
	v_rcp_f32_e32 v45, v36
	v_rcp_f32_e32 v46, v37
	s_waitcnt lgkmcnt(0)
	v_rcp_f32_e32 v47, v38
	ds_read_b128 v[34:37], v42 offset:49344
	v_rcp_f32_e32 v48, v39
	v_rcp_f32_e32 v49, v40
	v_rcp_f32_e32 v50, v41
	ds_read_b128 v[38:41], v42 offset:49376
	v_lshlrev_b32_e32 v42, 9, v189
	v_lshlrev_b32_e32 v51, 1, v188
	v_mul_f32_e32 v2, v2, v43
	v_add3_u32 v42, s6, v42, v51
	v_cvt_pk_bf16_f32 v2, v2, s0
	ds_write_b16 v42, v2 offset:51200
	v_mul_f32_e32 v2, v18, v43
	v_cvt_pk_bf16_f32 v2, v2, s0
	ds_write_b16 v42, v2 offset:51264
	v_mul_f32_e32 v2, v3, v44
	v_cvt_pk_bf16_f32 v2, v2, s0
	ds_write_b16 v42, v2 offset:51328
	v_mul_f32_e32 v2, v19, v44
	v_cvt_pk_bf16_f32 v2, v2, s0
	ds_write_b16 v42, v2 offset:51392
	v_mul_f32_e32 v2, v4, v45
	v_cvt_pk_bf16_f32 v2, v2, s0
	ds_write_b16 v42, v2 offset:51456
	v_mul_f32_e32 v2, v20, v45
	v_cvt_pk_bf16_f32 v2, v2, s0
	ds_write_b16 v42, v2 offset:51520
	v_mul_f32_e32 v2, v5, v46
	v_cvt_pk_bf16_f32 v2, v2, s0
	ds_write_b16 v42, v2 offset:51584
	v_mul_f32_e32 v2, v21, v46
	v_cvt_pk_bf16_f32 v2, v2, s0
	ds_write_b16 v42, v2 offset:51648
	v_mul_f32_e32 v2, v6, v47
	v_cvt_pk_bf16_f32 v2, v2, s0
	ds_write_b16 v42, v2 offset:52224
	v_mul_f32_e32 v2, v22, v47
	v_cvt_pk_bf16_f32 v2, v2, s0
	ds_write_b16 v42, v2 offset:52288
	v_mul_f32_e32 v2, v7, v48
	v_cvt_pk_bf16_f32 v2, v2, s0
	ds_write_b16 v42, v2 offset:52352
	v_mul_f32_e32 v2, v23, v48
	v_cvt_pk_bf16_f32 v2, v2, s0
	ds_write_b16 v42, v2 offset:52416
	v_mul_f32_e32 v2, v8, v49
	v_cvt_pk_bf16_f32 v2, v2, s0
	ds_write_b16 v42, v2 offset:52480
	v_mul_f32_e32 v2, v24, v49
	v_cvt_pk_bf16_f32 v2, v2, s0
	s_waitcnt lgkmcnt(14)
	v_rcp_f32_e32 v34, v34
	ds_write_b16 v42, v2 offset:52544
	v_mul_f32_e32 v2, v9, v50
	v_cvt_pk_bf16_f32 v2, v2, s0
	ds_write_b16 v42, v2 offset:52608
	v_mul_f32_e32 v2, v25, v50
	v_cvt_pk_bf16_f32 v2, v2, s0
	v_rcp_f32_e32 v35, v35
	ds_write_b16 v42, v2 offset:52672
	v_mul_f32_e32 v2, v10, v34
	v_cvt_pk_bf16_f32 v2, v2, s0
	ds_write_b16 v42, v2 offset:53248
	v_mul_f32_e32 v2, v26, v34
	v_cvt_pk_bf16_f32 v2, v2, s0
	v_rcp_f32_e32 v36, v36
	ds_write_b16 v42, v2 offset:53312
	v_mul_f32_e32 v2, v11, v35
	v_cvt_pk_bf16_f32 v2, v2, s0
	ds_write_b16 v42, v2 offset:53376
	v_mul_f32_e32 v2, v27, v35
	v_cvt_pk_bf16_f32 v2, v2, s0
	v_rcp_f32_e32 v37, v37
	ds_write_b16 v42, v2 offset:53440
	v_mul_f32_e32 v2, v12, v36
	v_cvt_pk_bf16_f32 v2, v2, s0
	ds_write_b16 v42, v2 offset:53504
	v_mul_f32_e32 v2, v28, v36
	v_cvt_pk_bf16_f32 v2, v2, s0
	s_waitcnt lgkmcnt(14)
	v_rcp_f32_e32 v38, v38
	ds_write_b16 v42, v2 offset:53568
	v_mul_f32_e32 v2, v13, v37
	v_cvt_pk_bf16_f32 v2, v2, s0
	ds_write_b16 v42, v2 offset:53632
	v_mul_f32_e32 v2, v29, v37
	v_cvt_pk_bf16_f32 v2, v2, s0
	v_rcp_f32_e32 v39, v39
	ds_write_b16 v42, v2 offset:53696
	v_mul_f32_e32 v2, v14, v38
	v_cvt_pk_bf16_f32 v2, v2, s0
	ds_write_b16 v42, v2 offset:54272
	v_mul_f32_e32 v2, v30, v38
	v_cvt_pk_bf16_f32 v2, v2, s0
	v_rcp_f32_e32 v40, v40
	ds_write_b16 v42, v2 offset:54336
	v_mul_f32_e32 v2, v15, v39
	v_cvt_pk_bf16_f32 v2, v2, s0
	ds_write_b16 v42, v2 offset:54400
	v_mul_f32_e32 v2, v31, v39
	v_cvt_pk_bf16_f32 v2, v2, s0
	v_rcp_f32_e32 v41, v41
	ds_write_b16 v42, v2 offset:54464
	v_mul_f32_e32 v2, v16, v40
	v_cvt_pk_bf16_f32 v2, v2, s0
	ds_write_b16 v42, v2 offset:54528
	v_mul_f32_e32 v2, v32, v40
	v_cvt_pk_bf16_f32 v2, v2, s0
	ds_write_b16 v42, v2 offset:54592
	v_mul_f32_e32 v2, v17, v41
	v_cvt_pk_bf16_f32 v2, v2, s0
	ds_write_b16 v42, v2 offset:54656
	v_mul_f32_e32 v2, v33, v41
	v_cvt_pk_bf16_f32 v2, v2, s0
	ds_write_b16 v42, v2 offset:54720
	v_lshlrev_b32_e32 v2, 1, v187
	v_and_b32_e32 v182, 0x70, v2
	v_lshrrev_b32_e32 v1, 3, v1
	v_add_u32_e32 v14, s6, v182
	s_waitcnt lgkmcnt(0)
	v_lshl_add_u32 v2, v1, 7, v14
	v_or_b32_e32 v15, 8, v1
	ds_read_b128 v[2:5], v2 offset:51200
	v_lshl_add_u32 v6, v15, 7, v14
	s_add_u32 s2, s39, s2
	ds_read_b128 v[6:9], v6 offset:51200
	s_addc_u32 s3, s40, s3
	v_lshl_add_u64 v[10:11], s[2:3], 0, v[182:183]
	v_lshlrev_b32_e32 v182, 11, v1
	v_lshl_add_u64 v[12:13], v[10:11], 0, v[182:183]
	v_lshlrev_b32_e32 v182, 11, v15
	s_waitcnt lgkmcnt(1)
	global_store_dwordx4 v[12:13], v[2:5], off
	s_mov_b64 s[2:3], 0
	s_nop 0
	v_lshl_add_u64 v[2:3], v[10:11], 0, v[182:183]
	s_waitcnt lgkmcnt(0)
	global_store_dwordx4 v[2:3], v[6:9], off
	s_nop 1
	v_or_b32_e32 v6, 16, v1
	v_lshl_add_u32 v2, v6, 7, v14
	v_or_b32_e32 v1, 24, v1
	ds_read_b128 v[2:5], v2 offset:51200
	v_lshlrev_b32_e32 v182, 11, v6
	v_lshl_add_u32 v6, v1, 7, v14
	ds_read_b128 v[6:9], v6 offset:51200
	v_lshl_add_u64 v[12:13], v[10:11], 0, v[182:183]
	v_lshlrev_b32_e32 v182, 11, v1
	s_waitcnt lgkmcnt(1)
	global_store_dwordx4 v[12:13], v[2:5], off
	s_nop 1
	v_lshl_add_u64 v[2:3], v[10:11], 0, v[182:183]
	s_waitcnt lgkmcnt(0)
	global_store_dwordx4 v[2:3], v[6:9], off
	s_waitcnt lgkmcnt(0)
	s_barrier

.LBB0_724:
	s_waitcnt lgkmcnt(14)
	v_mfma_f32_32x32x16_bf16 v[2:17], v[134:137], v[178:181], v[2:17]
	v_exp_f32_e32 v98, v98
	v_exp_f32_e32 v99, v99
	v_exp_f32_e32 v100, v100
	v_exp_f32_e32 v101, v101
	s_waitcnt lgkmcnt(12)
	v_mfma_f32_32x32x16_bf16 v[18:33], v[134:137], v[174:177], v[18:33]
	v_exp_f32_e32 v102, v102
	v_exp_f32_e32 v103, v103
	v_exp_f32_e32 v104, v104
	v_exp_f32_e32 v105, v105
	v_add_u32_e32 v78, s27, v206
	ds_read_b128 v[62:65], v78
	ds_read_b128 v[174:177], v78 offset:512
	s_waitcnt lgkmcnt(12)
	v_mfma_f32_32x32x16_bf16 v[2:17], v[126:129], v[66:69], v[2:17]
	v_exp_f32_e32 v106, v106
	v_exp_f32_e32 v107, v107
	v_exp_f32_e32 v108, v108
	v_exp_f32_e32 v109, v109
	ds_read_b128 v[178:181], v78 offset:2048
	ds_read_b128 v[170:173], v78 offset:2560
	s_waitcnt lgkmcnt(12)
	v_mfma_f32_32x32x16_bf16 v[18:33], v[126:129], v[70:73], v[18:33]
	v_exp_f32_e32 v110, v110
	v_exp_f32_e32 v111, v111
	v_exp_f32_e32 v112, v112
	v_exp_f32_e32 v113, v113
	ds_read_b128 v[166:169], v78 offset:4096
	ds_read_b128 v[162:165], v78 offset:4608
	s_waitcnt lgkmcnt(12)
	v_mfma_f32_32x32x16_bf16 v[2:17], v[118:121], v[74:77], v[2:17]
	v_exp_f32_e32 v82, v82
	v_exp_f32_e32 v83, v83
	v_exp_f32_e32 v84, v84
	v_exp_f32_e32 v85, v85
	ds_read_b128 v[158:161], v78 offset:6144
	ds_read_b128 v[154:157], v78 offset:6656
	s_waitcnt lgkmcnt(12)
	v_mfma_f32_32x32x16_bf16 v[18:33], v[118:121], v[50:53], v[18:33]
	v_exp_f32_e32 v86, v86
	v_exp_f32_e32 v87, v87
	v_exp_f32_e32 v88, v88
	v_exp_f32_e32 v89, v89
	s_waitcnt lgkmcnt(10)
	v_mfma_f32_32x32x16_bf16 v[2:17], v[114:117], v[54:57], v[2:17]
	v_exp_f32_e32 v90, v90
	v_exp_f32_e32 v91, v91
	v_exp_f32_e32 v92, v92
	v_exp_f32_e32 v93, v93
	s_waitcnt lgkmcnt(8)
	v_mfma_f32_32x32x16_bf16 v[18:33], v[114:117], v[58:61], v[18:33]
	v_exp_f32_e32 v94, v94
	v_exp_f32_e32 v95, v95
	v_exp_f32_e32 v96, v96
	v_exp_f32_e32 v97, v97
	s_cmp_lg_u32 s101, 0
	s_cbranch_scc1 .Lah_w7_b
	s_waitcnt vmcnt(2) lgkmcnt(0)
	s_branch .Lah_wd_b

.Lah_wd_b:
	s_barrier
	s_andn2_b64 vcc, exec, s[2:3]
	s_cbranch_vccnz .LBB0_726
	s_waitcnt lgkmcnt(0)
	v_add_u32_e32 v66, s43, v203
	ds_read_b128 v[50:53], v66 offset:49248
	ds_read_b128 v[54:57], v66 offset:49216
	ds_read_b128 v[58:61], v66 offset:49184
	ds_read_b128 v[66:69], v66 offset:49152
	s_waitcnt lgkmcnt(3)
	v_pk_mul_f32 v[14:15], v[14:15], v[50:51]
	s_waitcnt lgkmcnt(2)
	v_pk_mul_f32 v[10:11], v[10:11], v[54:55]
	s_waitcnt lgkmcnt(1)
	v_pk_mul_f32 v[6:7], v[6:7], v[58:59]
	v_pk_mul_f32 v[16:17], v[16:17], v[52:53]
	v_pk_mul_f32 v[12:13], v[12:13], v[56:57]
	v_pk_mul_f32 v[8:9], v[8:9], v[60:61]
	s_waitcnt lgkmcnt(0)
	v_pk_mul_f32 v[4:5], v[4:5], v[68:69]
	v_pk_mul_f32 v[2:3], v[2:3], v[66:67]
	v_pk_mul_f32 v[30:31], v[30:31], v[50:51]
	v_pk_mul_f32 v[26:27], v[26:27], v[54:55]
	v_pk_mul_f32 v[22:23], v[22:23], v[58:59]
	v_pk_mul_f32 v[32:33], v[32:33], v[52:53]
	v_pk_mul_f32 v[28:29], v[28:29], v[56:57]
	v_pk_mul_f32 v[24:25], v[24:25], v[60:61]
	v_pk_mul_f32 v[20:21], v[20:21], v[68:69]
	v_pk_mul_f32 v[18:19], v[18:19], v[66:67]

; #define WAIT_BAR(N) asm volatile("s_waitcnt vmcnt(" #N ") lgkmcnt(0)\n\ts_barrier":::"memory")
;   #define RESC() do{ if(resc){ asm volatile("s_waitcnt lgkmcnt(0)":::"memory"); \
;       _Pragma("unroll") for(int d_=0;d_<2;++d_) _Pragma("unroll") for(int r=0;r<16;++r)o[d_][r]*=wsf[crow(r,hi)]; } }while(0)
;   #define ROT() do{sl_prev=sl_cur;sl_cur=sl_next;sl_next=(sl_next==(NSLOT-1)*SLOTB)?0:sl_next+SLOTB;}while(0)
; #define GAS __attribute__((address_space(1)))
;     ...
;   int t=1;
;     ...
;   for(;t+5<NT;t+=2){
;     STEP(pB0,pB1,pA0,pA1,t,true,true,true);     WAIT_BAR(2); RESC(); ROT();
; __device__ __forceinline__ void f8w_finish(const F8WItem& it, f32x4 (&v)[16]) {
;     asm volatile("s_waitcnt vmcnt(0)" : "+v"(v[0]), "+v"(v[1]), "+v"(v[2]), "+v"(v[3]), "+v"(v[4]), "+v"(v[5]), "+v"(v[6]), "+v"(v[7]),
;                  "+v"(v[8]), "+v"(v[9]), "+v"(v[10]), "+v"(v[11]), "+v"(v[12]), "+v"(v[13]), "+v"(v[14]), "+v"(v[15]) :: "memory");
; #pragma unroll
;     for (int j = 0; j < 4; ++j) { v4u o;
;         o.x = pk4_f8(v[0][j] * W8_SCALE, v[1][j] * W8_SCALE, v[2][j] * W8_SCALE, v[3][j] * W8_SCALE); o.y = pk4_f8(v[4][j] * W8_SCALE, v[5][j] * W8_SCALE, v[6][j] * W8_SCALE, v[7][j] * W8_SCALE);
;         o.z = pk4_f8(v[8][j] * W8_SCALE, v[9][j] * W8_SCALE, v[10][j] * W8_SCALE, v[11][j] * W8_SCALE); o.w = pk4_f8(v[12][j] * W8_SCALE, v[13][j] * W8_SCALE, v[14][j] * W8_SCALE, v[15][j] * W8_SCALE);
;         *(GAS v4u*)(it.dst + j * 64) = o; }
; }
.LBB0_727:
	s_waitcnt lgkmcnt(14)
	v_mfma_f32_32x32x16_bf16 v[2:17], v[134:137], v[150:153], v[2:17]
	v_exp_f32_e32 v66, v66
	v_exp_f32_e32 v67, v67
	v_exp_f32_e32 v68, v68
	v_exp_f32_e32 v69, v69
	s_waitcnt lgkmcnt(12)
	v_mfma_f32_32x32x16_bf16 v[18:33], v[134:137], v[146:149], v[18:33]
	v_exp_f32_e32 v70, v70
	v_exp_f32_e32 v71, v71
	v_exp_f32_e32 v72, v72
	v_exp_f32_e32 v73, v73
	v_add_u32_e32 v94, s29, v206
	ds_read_b128 v[174:177], v94
	ds_read_b128 v[170:173], v94 offset:512
	s_waitcnt lgkmcnt(12)
	v_mfma_f32_32x32x16_bf16 v[2:17], v[126:129], v[98:101], v[2:17]
	v_exp_f32_e32 v74, v74
	v_exp_f32_e32 v75, v75
	v_exp_f32_e32 v76, v76
	v_exp_f32_e32 v77, v77
	ds_read_b128 v[166:169], v94 offset:2048
	ds_read_b128 v[162:165], v94 offset:2560
	s_waitcnt lgkmcnt(12)
	v_mfma_f32_32x32x16_bf16 v[18:33], v[126:129], v[102:105], v[18:33]
	v_exp_f32_e32 v78, v78
	v_exp_f32_e32 v79, v79
	v_exp_f32_e32 v80, v80
	v_exp_f32_e32 v81, v81
	ds_read_b128 v[158:161], v94 offset:4096
	ds_read_b128 v[154:157], v94 offset:4608
	s_waitcnt lgkmcnt(12)
	v_mfma_f32_32x32x16_bf16 v[2:17], v[118:121], v[106:109], v[2:17]
	v_exp_f32_e32 v50, v50
	v_exp_f32_e32 v51, v51
	v_exp_f32_e32 v52, v52
	v_exp_f32_e32 v53, v53
	ds_read_b128 v[150:153], v94 offset:6144
	ds_read_b128 v[146:149], v94 offset:6656
	s_waitcnt lgkmcnt(12)
	v_mfma_f32_32x32x16_bf16 v[18:33], v[118:121], v[82:85], v[18:33]
	v_exp_f32_e32 v54, v54
	v_exp_f32_e32 v55, v55
	v_exp_f32_e32 v56, v56
	v_exp_f32_e32 v57, v57
	s_waitcnt lgkmcnt(10)
	v_mfma_f32_32x32x16_bf16 v[2:17], v[114:117], v[86:89], v[2:17]
	v_exp_f32_e32 v58, v58
	v_exp_f32_e32 v59, v59
	v_exp_f32_e32 v60, v60
	v_exp_f32_e32 v61, v61
	s_waitcnt lgkmcnt(8)
	v_mfma_f32_32x32x16_bf16 v[18:33], v[114:117], v[90:93], v[18:33]
	v_exp_f32_e32 v62, v62
	v_exp_f32_e32 v63, v63
	v_exp_f32_e32 v64, v64
	v_exp_f32_e32 v65, v65
	s_waitcnt vmcnt(2) lgkmcnt(0)
	s_barrier
	s_cmp_lg_u32 s101, 0
	s_cbranch_scc0 .Lah_skip_b
	s_lshr_b32 s98, s82, 2
	s_mul_i32 s98, s98, 5
	s_add_i32 s99, s98, 2
	s_add_i32 s100, s98, 3
	s_and_b32 s93, s82, 3
	v_readlane_b32 s84, v244, s99
	v_readlane_b32 s85, v244, s100
	s_lshl_b32 s93, s93, 2
	v_mul_f32_e32 v210, 0x42800000, v210
	v_mul_f32_e32 v211, 0x42800000, v211
	v_mul_f32_e32 v212, 0x42800000, v212
	v_mul_f32_e32 v213, 0x42800000, v213
	v_mul_f32_e32 v214, 0x42800000, v214
	v_mul_f32_e32 v215, 0x42800000, v215
	v_mul_f32_e32 v216, 0x42800000, v216
	v_mul_f32_e32 v217, 0x42800000, v217
	v_mul_f32_e32 v218, 0x42800000, v218
	v_mul_f32_e32 v219, 0x42800000, v219
	v_mul_f32_e32 v220, 0x42800000, v220
	v_mul_f32_e32 v221, 0x42800000, v221
	v_mul_f32_e32 v222, 0x42800000, v222
	v_mul_f32_e32 v223, 0x42800000, v223
	v_mul_f32_e32 v234, 0x42800000, v234
	v_mul_f32_e32 v235, 0x42800000, v235
	s_add_u32 s84, s84, s93
	s_addc_u32 s85, s85, 0
	v_med3_f32 v210, v210, s33, v226
	v_med3_f32 v211, v211, s33, v226
	v_med3_f32 v212, v212, s33, v226
	v_med3_f32 v213, v213, s33, v226
	v_med3_f32 v214, v214, s33, v226
	v_med3_f32 v215, v215, s33, v226
	v_med3_f32 v216, v216, s33, v226
	v_med3_f32 v217, v217, s33, v226
	v_med3_f32 v218, v218, s33, v226
	v_med3_f32 v219, v219, s33, v226
	v_med3_f32 v220, v220, s33, v226
	v_med3_f32 v221, v221, s33, v226
	v_med3_f32 v222, v222, s33, v226
	v_med3_f32 v223, v223, s33, v226
	v_med3_f32 v234, v234, s33, v226
	v_med3_f32 v235, v235, s33, v226
	v_cvt_pk_fp8_f32 v210, v210, v214
	v_cvt_pk_fp8_f32 v211, v211, v215
	v_cvt_pk_fp8_f32 v212, v212, v216
	v_cvt_pk_fp8_f32 v213, v213, v217
	v_cvt_pk_fp8_f32 v210, v218, v222 op_sel:[0,0,1]
	v_cvt_pk_fp8_f32 v211, v219, v223 op_sel:[0,0,1]
	v_cvt_pk_fp8_f32 v212, v220, v234 op_sel:[0,0,1]
	v_cvt_pk_fp8_f32 v213, v221, v235 op_sel:[0,0,1]
	global_store_dword v243, v210, s[84:85]
	global_store_dword v243, v211, s[84:85] offset:64
	global_store_dword v243, v212, s[84:85] offset:128
	global_store_dword v243, v213, s[84:85] offset:192
	s_add_i32 s82, s82, 1
.Lah_skip_b:
	s_add_i32 s32, s32, -1
	s_cmp_lt_i32 s32, 0
	s_cselect_b32 s32, 2, s32
	s_andn2_b64 vcc, exec, s[2:3]
	s_cbranch_vccnz .LBB0_729
	s_waitcnt lgkmcnt(0)
	v_add_u32_e32 v94, s43, v203
	ds_read_b128 v[82:85], v94 offset:49248
	ds_read_b128 v[86:89], v94 offset:49216
	ds_read_b128 v[90:93], v94 offset:49152
	ds_read_b128 v[94:97], v94 offset:49184
	s_waitcnt lgkmcnt(3)
	v_pk_mul_f32 v[16:17], v[16:17], v[84:85]
	v_pk_mul_f32 v[14:15], v[14:15], v[82:83]
	s_waitcnt lgkmcnt(2)
	v_pk_mul_f32 v[12:13], v[12:13], v[88:89]
	v_pk_mul_f32 v[10:11], v[10:11], v[86:87]
	s_waitcnt lgkmcnt(0)
	v_pk_mul_f32 v[8:9], v[8:9], v[96:97]
	v_pk_mul_f32 v[6:7], v[6:7], v[94:95]
	v_pk_mul_f32 v[4:5], v[4:5], v[92:93]
	v_pk_mul_f32 v[2:3], v[2:3], v[90:91]
	v_pk_mul_f32 v[32:33], v[32:33], v[84:85]
	v_pk_mul_f32 v[30:31], v[30:31], v[82:83]
	v_pk_mul_f32 v[28:29], v[28:29], v[88:89]
	v_pk_mul_f32 v[26:27], v[26:27], v[86:87]
	v_pk_mul_f32 v[24:25], v[24:25], v[96:97]
	v_pk_mul_f32 v[22:23], v[22:23], v[94:95]
	v_pk_mul_f32 v[20:21], v[20:21], v[92:93]
	v_pk_mul_f32 v[18:19], v[18:19], v[90:91]

; #define GAS __attribute__((address_space(1)))
; __device__ __forceinline__ void f8w_load(const F8WItem& it, f32x4 (&v)[16]) {
; #pragma unroll
;     for (int i = 0; i < 16; ++i) { const GAS float* a = it.src + (size_t)i * it.ld; asm volatile("global_load_dwordx4 %0, %1, off nt" : "=v"(v[i]) : "v"(a) : "memory"); }
; }
; __device__ __forceinline__ void f8w_finish(const F8WItem& it, f32x4 (&v)[16]) {
;     asm volatile("s_waitcnt vmcnt(0)" : "+v"(v[0]), "+v"(v[1]), "+v"(v[2]), "+v"(v[3]), "+v"(v[4]), "+v"(v[5]), "+v"(v[6]), "+v"(v[7]),
;                  "+v"(v[8]), "+v"(v[9]), "+v"(v[10]), "+v"(v[11]), "+v"(v[12]), "+v"(v[13]), "+v"(v[14]), "+v"(v[15]) :: "memory");
; #pragma unroll
;     for (int j = 0; j < 4; ++j) { v4u o;
;         o.x = pk4_f8(v[0][j] * W8_SCALE, v[1][j] * W8_SCALE, v[2][j] * W8_SCALE, v[3][j] * W8_SCALE); o.y = pk4_f8(v[4][j] * W8_SCALE, v[5][j] * W8_SCALE, v[6][j] * W8_SCALE, v[7][j] * W8_SCALE);
;         o.z = pk4_f8(v[8][j] * W8_SCALE, v[9][j] * W8_SCALE, v[10][j] * W8_SCALE, v[11][j] * W8_SCALE); o.w = pk4_f8(v[12][j] * W8_SCALE, v[13][j] * W8_SCALE, v[14][j] * W8_SCALE, v[15][j] * W8_SCALE);
;         *(GAS v4u*)(it.dst + j * 64) = o; }
; }
.Lah_fb:
	s_cmp_lt_u32 s82, s83
	s_cbranch_scc0 .LBB0_773
	s_mov_b32 s93, s82
	s_lshr_b32 s98, s93, 2
	s_mul_i32 s98, s98, 5
	s_and_b32 s93, s93, 3
	s_add_i32 s99, s98, 1
	s_add_i32 s100, s98, 4
	v_readlane_b32 s84, v244, s98
	v_readlane_b32 s85, v244, s99
	v_readlane_b32 s99, v244, s100
	v_and_b32_e32 v246, 48, v243
	v_lshrrev_b32_e32 v209, 4, v243
	s_mul_i32 s100, s99, s93
	s_lshl_b32 s100, s100, 2
	s_add_u32 s84, s84, s100
	s_addc_u32 s85, s85, 0
	v_mul_u32_u24_e32 v246, s99, v246
	v_and_b32_e32 v209, 0xf0, v209
	v_add_u32_e32 v246, v246, v209
	s_nop 0
	global_load_dwordx4 v[210:213], v246, s[84:85] nt
	s_add_u32 s84, s84, s99
	s_addc_u32 s85, s85, 0
	global_load_dwordx4 v[214:217], v246, s[84:85] nt
	s_add_u32 s84, s84, s99
	s_addc_u32 s85, s85, 0
	global_load_dwordx4 v[218:221], v246, s[84:85] nt
	s_add_u32 s84, s84, s99
	s_addc_u32 s85, s85, 0
	global_load_dwordx2 v[222:223], v246, s[84:85] nt
	global_load_dwordx2 v[234:235], v246, s[84:85] offset:8 nt
	s_waitcnt vmcnt(0)
	s_lshr_b32 s98, s82, 2
	s_mul_i32 s98, s98, 5
	s_add_i32 s99, s98, 2
	s_add_i32 s100, s98, 3
	s_and_b32 s93, s82, 3
	v_readlane_b32 s84, v244, s99
	v_readlane_b32 s85, v244, s100
	s_lshl_b32 s93, s93, 2
	v_mul_f32_e32 v210, 0x42800000, v210
	v_mul_f32_e32 v211, 0x42800000, v211
	v_mul_f32_e32 v212, 0x42800000, v212
	v_mul_f32_e32 v213, 0x42800000, v213
	v_mul_f32_e32 v214, 0x42800000, v214
	v_mul_f32_e32 v215, 0x42800000, v215
	v_mul_f32_e32 v216, 0x42800000, v216
	v_mul_f32_e32 v217, 0x42800000, v217
	v_mul_f32_e32 v218, 0x42800000, v218
	v_mul_f32_e32 v219, 0x42800000, v219
	v_mul_f32_e32 v220, 0x42800000, v220
	v_mul_f32_e32 v221, 0x42800000, v221
	v_mul_f32_e32 v222, 0x42800000, v222
	v_mul_f32_e32 v223, 0x42800000, v223
	v_mul_f32_e32 v234, 0x42800000, v234
	v_mul_f32_e32 v235, 0x42800000, v235
	s_add_u32 s84, s84, s93
	s_addc_u32 s85, s85, 0
	v_med3_f32 v210, v210, s33, v226
	v_med3_f32 v211, v211, s33, v226
	v_med3_f32 v212, v212, s33, v226
	v_med3_f32 v213, v213, s33, v226
	v_med3_f32 v214, v214, s33, v226
	v_med3_f32 v215, v215, s33, v226
	v_med3_f32 v216, v216, s33, v226
	v_med3_f32 v217, v217, s33, v226
	v_med3_f32 v218, v218, s33, v226
	v_med3_f32 v219, v219, s33, v226
	v_med3_f32 v220, v220, s33, v226
	v_med3_f32 v221, v221, s33, v226
	v_med3_f32 v222, v222, s33, v226
	v_med3_f32 v223, v223, s33, v226
	v_med3_f32 v234, v234, s33, v226
	v_med3_f32 v235, v235, s33, v226
	v_cvt_pk_fp8_f32 v210, v210, v214
	v_cvt_pk_fp8_f32 v211, v211, v215
	v_cvt_pk_fp8_f32 v212, v212, v216
	v_cvt_pk_fp8_f32 v213, v213, v217
	v_cvt_pk_fp8_f32 v210, v218, v222 op_sel:[0,0,1]
	v_cvt_pk_fp8_f32 v211, v219, v223 op_sel:[0,0,1]
	v_cvt_pk_fp8_f32 v212, v220, v234 op_sel:[0,0,1]
	v_cvt_pk_fp8_f32 v213, v221, v235 op_sel:[0,0,1]
	global_store_dword v243, v210, s[84:85]
	global_store_dword v243, v211, s[84:85] offset:64
	global_store_dword v243, v212, s[84:85] offset:128
	global_store_dword v243, v213, s[84:85] offset:192
	s_add_i32 s82, s82, 1
	s_branch .Lah_fb
